# router: 12 of the 16 lo-weight operand fragments kept resident in unused VGPRs for the whole phase, the other 4 loaded per group ahead of the (now unconditional) next-row prefetch; counted waits no lo
# speedup vs baseline: 1.0200x; 1.0103x over previous
; #define LAS __attribute__((address_space(3)))
; __global__ void __launch_bounds__(NTHR, 2) mk_fwd(Args args) {
;     ...
;             const bf16* wrt_hi = WSP(bf16, WS_WRT) + (size_t)l * 65536; const bf16* wrt_lo = wrt_hi + 32768;
;             const float* br = router_b + l * NEXP; const float* g = norm2_g + l * DM;
;             constexpr int TP = 2064;
;             LAS unsigned char* Thi = lds; LAS unsigned char* Tlo = lds + 32 * TP; LAS unsigned char* PART = lds + 64 * TP; LAS float* LOG = (LAS float*)(lds + 64 * TP + 4096);
;             static_assert(64 * TP + 8192 <= LDS_CTL, "router LDS map");
;             const int eh = wave & 1, rh = (wave >> 1) & 1, kh = wave >> 2, n16 = lane & 15, q4 = lane >> 4;
;             fa::bf16x8 ah[16];
; #pragma unroll
;             for (int st = 0; st < 16; ++st) { const int k = kh * 512 + 32 * st + 8 * q4;
;                 ah[st] = *(const fa::bf16x8*)(wrt_hi + (eh * 16 + n16) * DM + k); }
;             const bf16* alp = wrt_lo + (eh * 16 + n16) * DM + kh * 512 + 8 * q4;
;             const f32x4 brv = *(const f32x4*)(br + eh * 16 + 4 * q4);
;             if (tid < 32) lctl[tid] = 0;
;             __syncthreads();
;             u32x4 xq[4][2];
;             if (bx < nmoe / 32) {
; #pragma unroll
;                 for (int rr = 0; rr < 4; ++rr)
; #pragma unroll
;                     for (int j = 0; j < 2; ++j) xq[rr][j] = *(const u32x4*)(X1 + (size_t)(bx * 32 + wave * 4 + rr) * DM + lane * 16 + 8 * j);
;             }
;             for (int grp = bx; grp < nmoe / 32; grp += G) {
.LBB0_660:
	s_andn2_b64 vcc, exec, s[14:15]
	s_cbranch_vccnz .LBB0_703
	s_lshl_b32 s14, s9, 4
	s_add_u32 s22, s20, 0x33c00000
	s_addc_u32 s23, s21, 0
	v_or_b32_e32 v105, s14, v118
	s_add_u32 s24, s20, 0x33a00000
	v_lshlrev_b32_e32 v120, 11, v105
	v_mov_b32_e32 v121, 0
	s_addc_u32 s25, s21, 0
	v_lshl_add_u64 v[108:109], s[20:21], 0, v[120:121]
	s_ashr_i32 s9, s8, 31
	v_lshl_add_u64 v[108:109], s[8:9], 1, v[108:109]
	v_lshlrev_b32_e32 v120, 1, v107
	v_lshl_add_u64 v[108:109], v[108:109], 0, v[120:121]
	s_mov_b64 s[8:9], 0x320000
	v_lshlrev_b32_e32 v124, 4, v103
	v_mov_b32_e32 v125, v121
	v_lshl_add_u64 v[122:123], v[108:109], 0, s[8:9]
	v_lshl_add_u64 v[108:109], s[20:21], 0, v[124:125]
	s_mov_b64 s[8:9], 0x19200000
	s_lshl_b32 s56, s59, 2
	v_lshl_add_u64 v[128:129], v[108:109], 0, s[8:9]
	s_add_i32 s8, 0, 0x10200
	s_lshr_b32 s9, s16, 3
	v_mov_b32_e32 v105, v121
	s_cmp_eq_u32 s17, 1
	s_load_dwordx2 s[10:11], s[10:11], 0x38
	v_lshlrev_b32_e32 v120, 6, v103
	v_add_u32_e32 v148, s8, v104
	v_lshl_add_u64 v[130:131], s[12:13], 0, v[104:105]
	v_and_or_b32 v103, s9, 16, v118
	s_movk_i32 s9, 0x810
	v_mov_b32_e32 v105, s8
	s_cselect_b64 s[26:27], -1, 0
	s_lshl_b32 s8, s59, 10
	v_add_u32_e32 v125, 0, v104
	v_mad_u32_u24 v104, v103, s9, 0
	v_mad_u32_u24 v103, v103, s9, v105
	s_and_b32 s9, s8, 0xc00
	s_add_i32 s58, 0, 0x20400
	s_add_i32 s57, s58, s9
	s_cmpk_lt_u32 s16, 0x100
	s_cselect_b64 s[28:29], -1, 0
	s_lshl_b32 s9, s16, 4
	s_waitcnt lgkmcnt(0)
	v_lshl_add_u64 v[126:127], s[10:11], 0, v[120:121]
	s_and_b32 s9, s9, 0xfffff800
	s_add_i32 s10, 0, 0x21400
	v_lshlrev_b32_e32 v110, 2, v106
	s_add_i32 s9, s10, s9
	s_lshl_b32 s11, s14, 2
	v_lshlrev_b32_e32 v105, 7, v118
	s_add_i32 s11, s11, s9
	v_lshlrev_b32_e32 v107, 2, v110
	v_add3_u32 v149, s11, v105, v107
	v_or_b32_e32 v105, s56, v106
	v_lshlrev_b32_e32 v105, 7, v105
	v_lshlrev_b32_e32 v150, 1, v118
	v_lshlrev_b32_e32 v107, 3, v118
	s_or_b32 s60, s56, 1
	v_lshlrev_b32_e32 v102, 1, v102
	s_add_i32 s16, s2, s64
	s_lshl_b32 s63, s2, 5
	s_add_i32 s58, s58, s8
	v_add3_u32 v151, s10, v105, v107
	v_or_b32_e32 v152, 1, v150
	v_cmp_gt_u32_e64 s[8:9], 4, v118
	v_cmp_eq_u32_e64 s[10:11], 0, v118
	v_cmp_eq_u32_e64 s[12:13], 1, v118
	v_cmp_eq_u32_e64 s[14:15], 2, v118
	s_mulk_i32 s59, 0x2040
	s_mulk_i32 s60, 0x810
	s_lshl_b32 s61, s16, 5
	s_lshl_b32 s62, s64, 5
	v_or_b32_e32 v153, s63, v106
	s_mov_b64 s[30:31], 0x104000
	s_mov_b64 s[34:35], 0x103000
	s_mov_b32 s65, 0x104000
	s_mov_b32 s66, 0x103000
	v_mov_b32_e32 v154, 0x358637bd
	v_add_u32_e32 v155, v104, v102
	v_add_u32_e32 v156, v103, v102
	v_mov_b32_e32 v157, 1
	v_mov_b32_e32 v158, 0xff61b1e6
	s_mov_b32 s67, s2
	global_load_dwordx4 v[206:209], v[122:123], off
	global_load_dwordx4 v[210:213], v[122:123], off offset:64
	global_load_dwordx4 v[214:217], v[122:123], off offset:128
	global_load_dwordx4 v[218:221], v[122:123], off offset:192
	global_load_dwordx4 v[222:225], v[122:123], off offset:256
	global_load_dwordx4 v[226:229], v[122:123], off offset:320
	global_load_dwordx4 v[230:233], v[122:123], off offset:384
	global_load_dwordx4 v[234:237], v[122:123], off offset:448
	global_load_dwordx4 v[238:241], v[122:123], off offset:512
	global_load_dwordx4 v[242:245], v[122:123], off offset:576
	global_load_dwordx4 v[246:249], v[122:123], off offset:640
	global_load_dwordx4 v[250:253], v[122:123], off offset:704
	s_branch .LBB0_663

; __global__ void __launch_bounds__(NTHR, 2) mk_fwd(Args args) {
;     ...
;             for (int grp = bx; grp < nmoe / 32; grp += G) {
;                 const int row0 = grp * 32; const int b = row0 < TL ? (row0 >> 12) : 16;
;                 const float* sh = modl + (size_t)b * (NMOD * DM) + 3 * DM; const float* sc = sh + DM;
;                 const int col = lane * 16;
;                 f32x4 gm[4], sv[4];
; #pragma unroll
;                 for (int j = 0; j < 4; ++j) { gm[j] = *(const f32x4*)(g + col + 4 * j) * (*(const f32x4*)(sc + col + 4 * j) + 1.0f); sv[j] = *(const f32x4*)(sh + col + 4 * j); }
; #pragma unroll
;                 for (int rr = 0; rr < 4; ++rr) {
;                     const int rl = wave * 4 + rr, row = row0 + rl; f32x4 v[4]; float ss = 0.f;
; #pragma unroll
;                     for (int j = 0; j < 2; ++j) { const u32x4 xb = xq[rr][j]; v[2 * j] = (f32x4){bflo(xb.x), bfhi(xb.x), bflo(xb.y), bfhi(xb.y)}; v[2 * j + 1] = (f32x4){bflo(xb.z), bfhi(xb.z), bflo(xb.w), bfhi(xb.w)}; }
; #pragma unroll
;                     for (int j = 0; j < 4; ++j) ss += (v[j].x * v[j].x + v[j].y * v[j].y) + (v[j].z * v[j].z + v[j].w * v[j].w);
;                     const float rstd = __builtin_amdgcn_rsqf(wave_sum(ss) * (1.0f / DM) + EPS);
.LBB0_663:
	s_min_i32 s16, s67, 0x800
	s_ashr_i32 s16, s16, 7
	s_mul_hi_i32 s17, s16, 0x6000
	s_mulk_i32 s16, 0x6000
	s_add_u32 s16, s20, s16
	s_addc_u32 s17, s21, s17
	v_lshlrev_b32_e32 v120, 2, v124
	v_lshl_add_u64 v[106:107], s[16:17], 0, v[120:121]
	v_add_co_u32_e32 v102, vcc, s65, v106
	v_lshl_add_u64 v[116:117], v[106:107], 0, s[34:35]
	s_nop 0
	v_addc_co_u32_e32 v103, vcc, 0, v107, vcc
	global_load_dwordx4 v[132:135], v[102:103], off
	v_lshl_add_u64 v[102:103], v[106:107], 0, s[30:31]
	global_load_dwordx4 v[136:139], v[102:103], off offset:16
	global_load_dwordx4 v[140:143], v[102:103], off offset:32
	global_load_dwordx4 v[160:163], v[126:127], off
	global_load_dwordx4 v[164:167], v[126:127], off offset:16
	global_load_dwordx4 v[168:171], v[126:127], off offset:32
	global_load_dwordx4 v[172:175], v[126:127], off offset:48
	global_load_dwordx4 v[176:179], v[102:103], off offset:48
	v_add_co_u32_e32 v102, vcc, s66, v106
	global_load_dwordx4 v[110:113], v[116:117], off offset:16
	s_nop 0
	v_addc_co_u32_e32 v103, vcc, 0, v107, vcc
	global_load_dwordx4 v[102:105], v[102:103], off
	s_waitcnt vmcnt(16)
	v_and_b32_e32 v187, 0xffff0000, v74
	v_and_b32_e32 v189, 0xffff0000, v75
	v_and_b32_e32 v193, 0xffff0000, v77
	v_and_b32_e32 v192, 0xffff0000, v76
	v_lshlrev_b32_e32 v181, 16, v72
	v_lshlrev_b32_e32 v186, 16, v74
	v_lshlrev_b32_e32 v188, 16, v75
	v_lshlrev_b32_e32 v191, 16, v77
	v_lshlrev_b32_e32 v190, 16, v76
	v_and_b32_e32 v197, 0xffff0000, v71
	v_mul_f32_e32 v108, v189, v189
	v_pk_mul_f32 v[114:115], v[192:193], v[192:193]
	v_mul_f32_e32 v106, v187, v187
	v_lshlrev_b32_e32 v196, 16, v71
	v_mov_b32_e32 v145, v181
	v_mul_f32_e32 v144, v197, v197
	v_pk_fma_f32 v[108:109], v[188:189], v[188:189], v[108:109] op_sel_hi:[1,1,0]
	v_pk_fma_f32 v[114:115], v[190:191], v[190:191], v[114:115]
	v_pk_fma_f32 v[106:107], v[186:187], v[186:187], v[106:107] op_sel_hi:[1,1,0]
	v_pk_fma_f32 v[198:199], v[196:197], v[196:197], v[144:145] op_sel_hi:[1,1,0]
	v_mov_b32_e32 v180, v106
	v_mov_b32_e32 v144, v108
	v_pk_add_f32 v[200:201], v[106:107], v[108:109]
	v_pk_add_f32 v[202:203], v[114:115], v[114:115] op_sel:[0,1] op_sel_hi:[1,0]
	global_load_dwordx4 v[106:109], v[116:117], off offset:48
	s_nop 0
	global_load_dwordx4 v[114:117], v[116:117], off offset:32
	v_and_b32_e32 v195, 0xffff0000, v70
	v_and_b32_e32 v183, 0xffff0000, v72
	v_lshlrev_b32_e32 v184, 16, v73
	v_and_b32_e32 v185, 0xffff0000, v73
	v_lshlrev_b32_e32 v194, 16, v70
	v_mul_f32_e32 v120, v195, v195
	v_mul_f32_e32 v159, v183, v183
	v_mul_f32_e32 v182, v184, v184
	v_mul_f32_e32 v204, v185, v185
	v_pk_fma_f32 v[146:147], v[194:195], v[194:195], v[120:121] op_sel_hi:[1,1,0]
	v_pk_mul_f32 v[144:145], v[180:181], v[144:145]
	v_mov_b32_e32 v147, v182
	v_mov_b32_e32 v199, v204
	v_mov_b32_e32 v203, v159
	v_mov_b32_e32 v201, v145
	v_pk_add_f32 v[146:147], v[146:147], v[198:199]
	v_pk_add_f32 v[144:145], v[200:201], v[202:203]
	v_mov_b32_e32 v182, v181
	v_pk_add_f32 v[144:145], v[144:145], v[146:147]
	v_add_u32_e32 v202, s60, v148
	v_add_f32_e32 v120, v144, v145
	s_add_i32 s67, s67, s64
	s_waitcnt vmcnt(10)
	v_pk_add_f32 v[136:137], v[136:137], 1.0 op_sel_hi:[1,0]
	v_add_f32_dpp v120, v120, v120 quad_perm:[1,0,3,2] row_mask:0xf bank_mask:0xf bound_ctrl:1
	v_pk_add_f32 v[138:139], v[138:139], 1.0 op_sel_hi:[1,0]
	s_waitcnt vmcnt(9)
	v_pk_add_f32 v[198:199], v[142:143], 1.0 op_sel_hi:[1,0]
	v_add_f32_dpp v120, v120, v120 quad_perm:[2,3,0,1] row_mask:0xf bank_mask:0xf bound_ctrl:1
	v_pk_add_f32 v[132:133], v[132:133], 1.0 op_sel_hi:[1,0]
	v_pk_add_f32 v[134:135], v[134:135], 1.0 op_sel_hi:[1,0]
	v_add_f32_dpp v120, v120, v120 row_half_mirror row_mask:0xf bank_mask:0xf bound_ctrl:1
	s_waitcnt vmcnt(8)
	v_pk_mul_f32 v[146:147], v[160:161], v[132:133]
	v_pk_mul_f32 v[144:145], v[162:163], v[134:135]
	v_add_f32_dpp v120, v120, v120 row_mirror row_mask:0xf bank_mask:0xf bound_ctrl:1
	s_waitcnt vmcnt(7)
	v_pk_mul_f32 v[142:143], v[164:165], v[136:137]
	v_readlane_b32 s44, v120, 16
	v_readlane_b32 s45, v120, 48
	v_readlane_b32 s16, v120, 0
	v_readlane_b32 s17, v120, 32
	v_mov_b32_e32 v132, s44
	v_mov_b32_e32 v133, s45
	v_pk_add_f32 v[132:133], s[16:17], v[132:133]
	v_pk_add_f32 v[200:201], v[140:141], 1.0 op_sel_hi:[1,0]
	v_add_f32_e32 v120, v132, v133
	v_fmamk_f32 v120, v120, 0x3a800000, v154
	v_rsq_f32_e32 v120, v120
	v_pk_mul_f32 v[140:141], v[166:167], v[138:139]
	s_waitcnt vmcnt(6)
	v_pk_mul_f32 v[136:137], v[168:169], v[200:201]
	s_waitcnt vmcnt(4)
	v_pk_add_f32 v[138:139], v[176:177], 1.0 op_sel_hi:[1,0]
	v_pk_mul_f32 v[160:161], v[120:121], v[186:187] op_sel_hi:[0,1]
	s_waitcnt vmcnt(2)
	v_pk_fma_f32 v[162:163], v[160:161], v[146:147], v[102:103]
	v_mov_b32_e32 v160, v121
	v_cvt_pk_fp8_f32 v160, v162, v163
	v_pk_mul_f32 v[164:165], v[120:121], v[188:189] op_sel_hi:[0,1]
	v_pk_fma_f32 v[166:167], v[164:165], v[144:145], v[104:105]
	v_cvt_pk_bf16_f32 v164, v162, v163
	v_pk_mul_f32 v[138:139], v[172:173], v[138:139]
	v_lshlrev_b32_e32 v159, 16, v164
	v_and_b32_e32 v161, 0xffff0000, v164
	v_sub_f32_e32 v159, v162, v159
	v_sub_f32_e32 v161, v163, v161
	v_cvt_pk_bf16_f32 v165, v166, v167
	v_cvt_pk_bf16_f32 v168, v159, v161
	v_mov_b32_e32 v162, v190
	v_lshlrev_b32_e32 v159, 16, v165
	v_and_b32_e32 v161, 0xffff0000, v165
	v_mov_b32_e32 v163, v192
	v_mov_b32_e32 v192, v191
	v_cvt_pk_fp8_f32 v160, v166, v167 op_sel:[0,0,1]
	v_sub_f32_e32 v159, v166, v159
	v_sub_f32_e32 v161, v167, v161
	v_pk_mul_f32 v[162:163], v[120:121], v[162:163] op_sel_hi:[0,1]
	v_pk_mul_f32 v[166:167], v[120:121], v[192:193] op_sel_hi:[0,1]
	v_cvt_pk_bf16_f32 v169, v159, v161
	v_pk_fma_f32 v[162:163], v[162:163], v[142:143], v[110:111]
	v_mov_b32_e32 v161, v121
	v_pk_fma_f32 v[172:173], v[166:167], v[140:141], v[112:113]
	v_cvt_pk_bf16_f32 v166, v162, v163
	v_cvt_pk_fp8_f32 v161, v162, v163
	v_lshlrev_b32_e32 v159, 16, v166
	v_sub_f32_e32 v159, v162, v159
	v_and_b32_e32 v162, 0xffff0000, v166
	v_sub_f32_e32 v162, v163, v162
	v_pk_mul_f32 v[134:135], v[170:171], v[198:199]
	v_cvt_pk_bf16_f32 v167, v172, v173
	v_cvt_pk_bf16_f32 v170, v159, v162
	v_pk_add_f32 v[132:133], v[178:179], 1.0 op_sel_hi:[1,0]
	v_and_b32_e32 v162, 0xffff0000, v167
	v_sub_f32_e32 v171, v173, v162
	v_pk_mul_f32 v[162:163], v[120:121], v[194:195] op_sel_hi:[0,1]
	v_pk_mul_f32 v[132:133], v[174:175], v[132:133]
	v_lshlrev_b32_e32 v159, 16, v167
	s_waitcnt vmcnt(0)
; __device__ __forceinline__ unsigned cvt_pk_bf16(float lo, float hi) { unsigned r; asm volatile("v_cvt_pk_bf16_f32 %0, %1, %2" : "=v"(r) : "v"(lo), "v"(hi)); return r; }
; __device__ __forceinline__ unsigned pk4_fp8(float a, float b, float c, float d) { int w = __builtin_amdgcn_cvt_pk_fp8_f32(a, b, 0, false); w = __builtin_amdgcn_cvt_pk_fp8_f32(c, d, w, true); return (unsigned)w; }
; #define LAS __attribute__((address_space(3)))
; __global__ void __launch_bounds__(NTHR, 2) mk_fwd(Args args) {
;     ...
;                 for (int rr = 0; rr < 4; ++rr) {
;                     const int rl = wave * 4 + rr, row = row0 + rl; f32x4 v[4]; float ss = 0.f;
; #pragma unroll
;                     for (int j = 0; j < 2; ++j) { const u32x4 xb = xq[rr][j]; v[2 * j] = (f32x4){bflo(xb.x), bfhi(xb.x), bflo(xb.y), bfhi(xb.y)}; v[2 * j + 1] = (f32x4){bflo(xb.z), bfhi(xb.z), bflo(xb.w), bfhi(xb.w)}; }
; #pragma unroll
;                     for (int j = 0; j < 4; ++j) ss += (v[j].x * v[j].x + v[j].y * v[j].y) + (v[j].z * v[j].z + v[j].w * v[j].w);
;                     const float rstd = __builtin_amdgcn_rsqf(wave_sum(ss) * (1.0f / DM) + EPS);
;                     u32x4 h8, hiw[2], low[2];
; #pragma unroll
;                     for (int j = 0; j < 4; ++j) {
;                         const f32x4 h = (v[j] * rstd) * gm[j] + sv[j];
;                         h8[j] = pk4_fp8(h.x, h.y, h.z, h.w);
;                         const unsigned h0 = pg8::cvt_pk_bf16(h.x, h.y), h1 = pg8::cvt_pk_bf16(h.z, h.w);
;                         hiw[j >> 1][2 * (j & 1)] = h0; hiw[j >> 1][2 * (j & 1) + 1] = h1;
;                         low[j >> 1][2 * (j & 1)] = pg8::cvt_pk_bf16(h.x - bflo(h0), h.y - bfhi(h0)); low[j >> 1][2 * (j & 1) + 1] = pg8::cvt_pk_bf16(h.z - bflo(h1), h.w - bfhi(h1));
;                     }
;                     *(u32x4*)((unsigned char*)H + (size_t)row * DM + col) = h8;
; #pragma unroll
;                     for (int j = 0; j < 2; ++j) { *(LAS u32x4*)(Thi + rl * TP + col * 2 + 16 * j) = hiw[j]; *(LAS u32x4*)(Tlo + rl * TP + col * 2 + 16 * j) = low[j]; }
;                 }
	v_pk_fma_f32 v[174:175], v[162:163], v[136:137], v[114:115]
	v_mov_b32_e32 v162, v121
	v_cvt_pk_fp8_f32 v161, v172, v173 op_sel:[0,0,1]
	v_sub_f32_e32 v159, v172, v159
	v_cvt_pk_fp8_f32 v162, v174, v175
	v_pk_mul_f32 v[172:173], v[120:121], v[196:197] op_sel_hi:[0,1]
	v_cvt_pk_bf16_f32 v171, v159, v171
	v_pk_fma_f32 v[178:179], v[172:173], v[134:135], v[116:117]
	v_cvt_pk_bf16_f32 v172, v174, v175
	s_add_i32 s16, s56, s63
	v_lshlrev_b32_e32 v159, 16, v172
	v_and_b32_e32 v163, 0xffff0000, v172
	v_sub_f32_e32 v159, v174, v159
	v_sub_f32_e32 v163, v175, v163
	v_cvt_pk_bf16_f32 v173, v178, v179
	v_cvt_pk_bf16_f32 v176, v159, v163
	v_pk_mul_f32 v[174:175], v[120:121], v[182:183] op_sel_hi:[0,1]
	v_lshlrev_b32_e32 v159, 16, v173
	v_and_b32_e32 v163, 0xffff0000, v173
	v_cvt_pk_fp8_f32 v162, v178, v179 op_sel:[0,0,1]
	v_sub_f32_e32 v159, v178, v159
	v_sub_f32_e32 v177, v179, v163
	v_pk_fma_f32 v[178:179], v[174:175], v[138:139], v[106:107]
	v_mov_b32_e32 v163, v121
	v_cvt_pk_fp8_f32 v163, v178, v179
	v_pk_mul_f32 v[174:175], v[120:121], v[184:185] op_sel_hi:[0,1]
	v_cvt_pk_bf16_f32 v177, v159, v177
	v_pk_fma_f32 v[180:181], v[174:175], v[132:133], v[108:109]
	v_cvt_pk_bf16_f32 v174, v178, v179
	s_ashr_i32 s17, s16, 31
	v_and_b32_e32 v159, 0xffff0000, v174
	v_lshlrev_b32_e32 v120, 16, v174
	v_sub_f32_e32 v159, v179, v159
	v_cvt_pk_fp8_f32 v163, v180, v181 op_sel:[0,0,1]
	v_cvt_pk_bf16_f32 v175, v180, v181
	v_sub_f32_e32 v120, v178, v120
	v_cvt_pk_bf16_f32 v178, v120, v159
	v_and_b32_e32 v159, 0xffff0000, v175
	v_lshlrev_b32_e32 v120, 16, v175
	v_sub_f32_e32 v159, v181, v159
	v_sub_f32_e32 v120, v180, v120
	v_cvt_pk_bf16_f32 v179, v120, v159
	s_lshl_b64 s[44:45], s[16:17], 10
	v_add_u32_e32 v159, s59, v125
	v_lshl_add_u64 v[180:181], v[128:129], 0, s[44:45]
	ds_write_b128 v159, v[164:167]
	v_and_b32_e32 v165, 0xffff0000, v83
	global_store_dwordx4 v[180:181], v[160:163], off
	v_lshlrev_b32_e32 v164, 16, v83
	v_mul_f32_e32 v120, v165, v165
	v_and_b32_e32 v161, 0xffff0000, v82
	v_lshlrev_b32_e32 v160, 16, v82
	v_pk_fma_f32 v[166:167], v[164:165], v[164:165], v[120:121] op_sel_hi:[1,1,0]
	v_and_b32_e32 v187, 0xffff0000, v85
	v_and_b32_e32 v186, 0xffff0000, v84
	v_mul_f32_e32 v120, v161, v161
	v_lshlrev_b32_e32 v163, 16, v80
	v_lshlrev_b32_e32 v185, 16, v85
	v_lshlrev_b32_e32 v184, 16, v84
	v_pk_mul_f32 v[188:189], v[186:187], v[186:187]
	v_pk_fma_f32 v[194:195], v[160:161], v[160:161], v[120:121] op_sel_hi:[1,1,0]
	v_and_b32_e32 v181, 0xffff0000, v80
	v_pk_fma_f32 v[188:189], v[184:185], v[184:185], v[188:189]
	v_mov_b32_e32 v162, v194
	v_mov_b32_e32 v196, v166
	v_mov_b32_e32 v197, v163
	v_and_b32_e32 v191, 0xffff0000, v78
	v_mul_f32_e32 v180, v181, v181
	v_pk_add_f32 v[166:167], v[194:195], v[166:167]
	v_pk_mul_f32 v[194:195], v[162:163], v[196:197]
	v_pk_add_f32 v[188:189], v[188:189], v[188:189] op_sel:[0,1] op_sel_hi:[1,0]
	v_lshlrev_b32_e32 v190, 16, v78
	v_and_b32_e32 v193, 0xffff0000, v79
	v_mov_b32_e32 v167, v195
	v_mov_b32_e32 v189, v180
	v_mul_f32_e32 v120, v191, v191
	v_lshlrev_b32_e32 v182, 16, v81
	v_and_b32_e32 v183, 0xffff0000, v81
	v_lshlrev_b32_e32 v192, 16, v79
	v_pk_add_f32 v[166:167], v[166:167], v[188:189]
	v_pk_fma_f32 v[188:189], v[190:191], v[190:191], v[120:121] op_sel_hi:[1,1,0]
	v_mul_f32_e32 v120, v193, v193
	v_mul_f32_e32 v198, v182, v182
	v_mul_f32_e32 v199, v183, v183
	v_pk_fma_f32 v[194:195], v[192:193], v[192:193], v[120:121] op_sel_hi:[1,1,0]
	v_mov_b32_e32 v189, v198
	v_mov_b32_e32 v195, v199
	v_pk_add_f32 v[188:189], v[188:189], v[194:195]
	v_add_u32_e32 v162, s59, v148
	v_pk_add_f32 v[166:167], v[166:167], v[188:189]
	ds_write_b128 v162, v[168:171]
	ds_write_b128 v159, v[172:175] offset:16
	v_add_f32_e32 v120, v166, v167
	ds_write_b128 v162, v[176:179] offset:16
	v_mov_b32_e32 v180, v163
	v_add_f32_dpp v120, v120, v120 quad_perm:[1,0,3,2] row_mask:0xf bank_mask:0xf bound_ctrl:1
	v_mov_b32_e32 v163, v121
	s_nop 0
	v_add_f32_dpp v120, v120, v120 quad_perm:[2,3,0,1] row_mask:0xf bank_mask:0xf bound_ctrl:1
	s_nop 1
	v_add_f32_dpp v120, v120, v120 row_half_mirror row_mask:0xf bank_mask:0xf bound_ctrl:1
	s_nop 1
	v_add_f32_dpp v120, v120, v120 row_mirror row_mask:0xf bank_mask:0xf bound_ctrl:1
	s_nop 0
	v_readlane_b32 s17, v120, 16
	v_readlane_b32 s46, v120, 48
	v_readlane_b32 s44, v120, 0
	v_readlane_b32 s45, v120, 32
	v_mov_b32_e32 v166, s17
	v_mov_b32_e32 v167, s46
	v_pk_add_f32 v[166:167], s[44:45], v[166:167]
	s_add_i32 s44, s16, 1
	v_add_f32_e32 v120, v166, v167
	v_fmamk_f32 v120, v120, 0x3a800000, v154
	v_rsq_f32_e32 v120, v120
	s_ashr_i32 s45, s44, 31
	s_lshl_b64 s[44:45], s[44:45], 10
	v_pk_mul_f32 v[160:161], v[120:121], v[160:161] op_sel_hi:[0,1]
	v_pk_fma_f32 v[166:167], v[160:161], v[146:147], v[102:103]
	v_mov_b32_e32 v160, v121
	v_pk_mul_f32 v[164:165], v[120:121], v[164:165] op_sel_hi:[0,1]
	v_cvt_pk_fp8_f32 v160, v166, v167
	v_pk_fma_f32 v[170:171], v[164:165], v[144:145], v[104:105]
	v_cvt_pk_bf16_f32 v164, v166, v167
	s_nop 0
	v_and_b32_e32 v161, 0xffff0000, v164
	v_lshlrev_b32_e32 v159, 16, v164
	v_sub_f32_e32 v161, v167, v161
	v_cvt_pk_bf16_f32 v165, v170, v171
	v_sub_f32_e32 v159, v166, v159
	v_cvt_pk_bf16_f32 v168, v159, v161
	v_and_b32_e32 v161, 0xffff0000, v165
	v_mov_b32_e32 v166, v184
	v_mov_b32_e32 v167, v186
	v_lshlrev_b32_e32 v159, 16, v165
	v_sub_f32_e32 v161, v171, v161
	v_pk_mul_f32 v[166:167], v[120:121], v[166:167] op_sel_hi:[0,1]
	v_cvt_pk_fp8_f32 v160, v170, v171 op_sel:[0,0,1]
	v_sub_f32_e32 v159, v170, v159
	v_cvt_pk_bf16_f32 v169, v159, v161
	v_pk_fma_f32 v[170:171], v[166:167], v[142:143], v[110:111]
	v_mov_b32_e32 v161, v121
	v_mov_b32_e32 v186, v185
	v_cvt_pk_fp8_f32 v161, v170, v171
; __device__ __forceinline__ unsigned cvt_pk_bf16(float lo, float hi) { unsigned r; asm volatile("v_cvt_pk_bf16_f32 %0, %1, %2" : "=v"(r) : "v"(lo), "v"(hi)); return r; }
; __device__ __forceinline__ unsigned pk4_fp8(float a, float b, float c, float d) { int w = __builtin_amdgcn_cvt_pk_fp8_f32(a, b, 0, false); w = __builtin_amdgcn_cvt_pk_fp8_f32(c, d, w, true); return (unsigned)w; }
; #define LAS __attribute__((address_space(3)))
; __global__ void __launch_bounds__(NTHR, 2) mk_fwd(Args args) {
;     ...
;                 for (int rr = 0; rr < 4; ++rr) {
;                     const int rl = wave * 4 + rr, row = row0 + rl; f32x4 v[4]; float ss = 0.f;
; #pragma unroll
;                     for (int j = 0; j < 2; ++j) { const u32x4 xb = xq[rr][j]; v[2 * j] = (f32x4){bflo(xb.x), bfhi(xb.x), bflo(xb.y), bfhi(xb.y)}; v[2 * j + 1] = (f32x4){bflo(xb.z), bfhi(xb.z), bflo(xb.w), bfhi(xb.w)}; }
; #pragma unroll
;                     for (int j = 0; j < 4; ++j) ss += (v[j].x * v[j].x + v[j].y * v[j].y) + (v[j].z * v[j].z + v[j].w * v[j].w);
;                     const float rstd = __builtin_amdgcn_rsqf(wave_sum(ss) * (1.0f / DM) + EPS);
;                     u32x4 h8, hiw[2], low[2];
; #pragma unroll
;                     for (int j = 0; j < 4; ++j) {
;                         const f32x4 h = (v[j] * rstd) * gm[j] + sv[j];
;                         h8[j] = pk4_fp8(h.x, h.y, h.z, h.w);
;                         const unsigned h0 = pg8::cvt_pk_bf16(h.x, h.y), h1 = pg8::cvt_pk_bf16(h.z, h.w);
;                         hiw[j >> 1][2 * (j & 1)] = h0; hiw[j >> 1][2 * (j & 1) + 1] = h1;
;                         low[j >> 1][2 * (j & 1)] = pg8::cvt_pk_bf16(h.x - bflo(h0), h.y - bfhi(h0)); low[j >> 1][2 * (j & 1) + 1] = pg8::cvt_pk_bf16(h.z - bflo(h1), h.w - bfhi(h1));
;                     }
;                     *(u32x4*)((unsigned char*)H + (size_t)row * DM + col) = h8;
; #pragma unroll
;                     for (int j = 0; j < 2; ++j) { *(LAS u32x4*)(Thi + rl * TP + col * 2 + 16 * j) = hiw[j]; *(LAS u32x4*)(Tlo + rl * TP + col * 2 + 16 * j) = low[j]; }
;                 }
	v_pk_mul_f32 v[166:167], v[120:121], v[186:187] op_sel_hi:[0,1]
	v_pk_fma_f32 v[172:173], v[166:167], v[140:141], v[112:113]
	v_cvt_pk_bf16_f32 v166, v170, v171
	v_and_b32_e32 v187, 0xffff0000, v93
	v_lshlrev_b32_e32 v159, 16, v166
	v_and_b32_e32 v162, 0xffff0000, v166
	v_sub_f32_e32 v159, v170, v159
	v_sub_f32_e32 v162, v171, v162
	v_cvt_pk_bf16_f32 v167, v172, v173
	v_cvt_pk_bf16_f32 v170, v159, v162
	v_cvt_pk_fp8_f32 v161, v172, v173 op_sel:[0,0,1]
	v_lshlrev_b32_e32 v159, 16, v167
	v_and_b32_e32 v162, 0xffff0000, v167
	v_sub_f32_e32 v159, v172, v159
	v_sub_f32_e32 v171, v173, v162
	v_pk_mul_f32 v[172:173], v[120:121], v[190:191] op_sel_hi:[0,1]
	v_pk_fma_f32 v[174:175], v[172:173], v[136:137], v[114:115]
	v_pk_mul_f32 v[172:173], v[120:121], v[192:193] op_sel_hi:[0,1]
	v_mov_b32_e32 v162, v121
	v_cvt_pk_bf16_f32 v171, v159, v171
	v_pk_fma_f32 v[178:179], v[172:173], v[134:135], v[116:117]
	v_cvt_pk_bf16_f32 v172, v174, v175
	v_cvt_pk_fp8_f32 v162, v174, v175
	v_lshlrev_b32_e32 v159, 16, v172
	v_sub_f32_e32 v159, v174, v159
	v_and_b32_e32 v174, 0xffff0000, v172
	v_sub_f32_e32 v174, v175, v174
	v_cvt_pk_bf16_f32 v173, v178, v179
	v_cvt_pk_bf16_f32 v176, v159, v174
	v_cvt_pk_fp8_f32 v162, v178, v179 op_sel:[0,0,1]
	v_and_b32_e32 v174, 0xffff0000, v173
	v_lshlrev_b32_e32 v159, 16, v173
	v_sub_f32_e32 v177, v179, v174
	v_pk_mul_f32 v[174:175], v[120:121], v[180:181] op_sel_hi:[0,1]
	v_sub_f32_e32 v159, v178, v159
	v_pk_fma_f32 v[178:179], v[174:175], v[138:139], v[106:107]
	v_pk_mul_f32 v[174:175], v[120:121], v[182:183] op_sel_hi:[0,1]
	v_cvt_pk_fp8_f32 v163, v178, v179
	v_cvt_pk_bf16_f32 v177, v159, v177
	v_pk_fma_f32 v[180:181], v[174:175], v[132:133], v[108:109]
	v_cvt_pk_bf16_f32 v174, v178, v179
	v_and_b32_e32 v186, 0xffff0000, v92
	v_and_b32_e32 v159, 0xffff0000, v174
	v_lshlrev_b32_e32 v120, 16, v174
	v_sub_f32_e32 v159, v179, v159
	v_cvt_pk_fp8_f32 v163, v180, v181 op_sel:[0,0,1]
	v_cvt_pk_bf16_f32 v175, v180, v181
	v_sub_f32_e32 v120, v178, v120
	v_cvt_pk_bf16_f32 v178, v120, v159
	v_and_b32_e32 v159, 0xffff0000, v175
	v_lshlrev_b32_e32 v120, 16, v175
	v_sub_f32_e32 v159, v181, v159
	v_sub_f32_e32 v120, v180, v120
	v_cvt_pk_bf16_f32 v179, v120, v159
	v_add_u32_e32 v159, s60, v125
	v_lshl_add_u64 v[180:181], v[128:129], 0, s[44:45]
	ds_write_b128 v159, v[164:167]
	v_and_b32_e32 v165, 0xffff0000, v91
	global_store_dwordx4 v[180:181], v[160:163], off
	v_lshlrev_b32_e32 v164, 16, v91
	v_mul_f32_e32 v120, v165, v165
	v_and_b32_e32 v161, 0xffff0000, v90
	v_lshlrev_b32_e32 v160, 16, v90
	v_pk_fma_f32 v[166:167], v[164:165], v[164:165], v[120:121] op_sel_hi:[1,1,0]
	v_mul_f32_e32 v120, v161, v161
	v_lshlrev_b32_e32 v163, 16, v88
	v_lshlrev_b32_e32 v185, 16, v93
	v_lshlrev_b32_e32 v184, 16, v92
	v_pk_mul_f32 v[188:189], v[186:187], v[186:187]
	v_pk_fma_f32 v[194:195], v[160:161], v[160:161], v[120:121] op_sel_hi:[1,1,0]
	v_and_b32_e32 v181, 0xffff0000, v88
	v_pk_fma_f32 v[188:189], v[184:185], v[184:185], v[188:189]
	v_mov_b32_e32 v162, v194
	v_mov_b32_e32 v196, v166
	v_mov_b32_e32 v197, v163
	v_and_b32_e32 v191, 0xffff0000, v86
	v_mul_f32_e32 v180, v181, v181
	v_pk_add_f32 v[166:167], v[194:195], v[166:167]
	v_pk_mul_f32 v[194:195], v[162:163], v[196:197]
	v_pk_add_f32 v[188:189], v[188:189], v[188:189] op_sel:[0,1] op_sel_hi:[1,0]
	v_lshlrev_b32_e32 v190, 16, v86
	v_and_b32_e32 v193, 0xffff0000, v87
	v_mov_b32_e32 v167, v195
	v_mov_b32_e32 v189, v180
	v_mul_f32_e32 v120, v191, v191
	v_lshlrev_b32_e32 v182, 16, v89
	v_and_b32_e32 v183, 0xffff0000, v89
	v_lshlrev_b32_e32 v192, 16, v87
	v_pk_add_f32 v[166:167], v[166:167], v[188:189]
	v_pk_fma_f32 v[188:189], v[190:191], v[190:191], v[120:121] op_sel_hi:[1,1,0]
	v_mul_f32_e32 v120, v193, v193
	v_mul_f32_e32 v198, v182, v182
	v_mul_f32_e32 v199, v183, v183
	v_pk_fma_f32 v[194:195], v[192:193], v[192:193], v[120:121] op_sel_hi:[1,1,0]
	v_mov_b32_e32 v189, v198
	v_mov_b32_e32 v195, v199
	v_pk_add_f32 v[188:189], v[188:189], v[194:195]
	ds_write_b128 v202, v[168:171]
	ds_write_b128 v159, v[172:175] offset:16
	v_pk_add_f32 v[166:167], v[166:167], v[188:189]
	ds_write_b128 v202, v[176:179] offset:16
	v_add_f32_e32 v120, v166, v167
	v_mov_b32_e32 v180, v163
	v_mov_b32_e32 v163, v121
	v_add_f32_dpp v120, v120, v120 quad_perm:[1,0,3,2] row_mask:0xf bank_mask:0xf bound_ctrl:1
	v_lshlrev_b32_e32 v189, 16, v101
	v_lshlrev_b32_e32 v188, 16, v100
	v_add_f32_dpp v120, v120, v120 quad_perm:[2,3,0,1] row_mask:0xf bank_mask:0xf bound_ctrl:1
	v_and_b32_e32 v195, 0xffff0000, v94
	v_lshlrev_b32_e32 v194, 16, v94
	v_add_f32_dpp v120, v120, v120 row_half_mirror row_mask:0xf bank_mask:0xf bound_ctrl:1
	v_and_b32_e32 v197, 0xffff0000, v95
	v_lshlrev_b32_e32 v196, 16, v95
	v_add_f32_dpp v120, v120, v120 row_mirror row_mask:0xf bank_mask:0xf bound_ctrl:1
	s_nop 0
	v_readlane_b32 s17, v120, 16
	v_readlane_b32 s46, v120, 48
	v_readlane_b32 s44, v120, 0
	v_readlane_b32 s45, v120, 32
	v_mov_b32_e32 v166, s17
	v_mov_b32_e32 v167, s46
	v_pk_add_f32 v[166:167], s[44:45], v[166:167]
	s_add_i32 s44, s16, 2
	v_add_f32_e32 v120, v166, v167
	v_fmamk_f32 v120, v120, 0x3a800000, v154
	v_rsq_f32_e32 v120, v120
	s_ashr_i32 s45, s44, 31
	s_lshl_b64 s[44:45], s[44:45], 10
	s_add_i32 s16, s16, 3
	v_pk_mul_f32 v[160:161], v[120:121], v[160:161] op_sel_hi:[0,1]
	v_pk_fma_f32 v[166:167], v[160:161], v[146:147], v[102:103]
	v_mov_b32_e32 v160, v121
	v_cvt_pk_fp8_f32 v160, v166, v167
	v_pk_mul_f32 v[164:165], v[120:121], v[164:165] op_sel_hi:[0,1]
	v_pk_fma_f32 v[170:171], v[164:165], v[144:145], v[104:105]
	v_cvt_pk_bf16_f32 v164, v166, v167
	s_nop 0
	v_lshlrev_b32_e32 v161, 16, v164
	v_and_b32_e32 v162, 0xffff0000, v164
; __device__ __forceinline__ unsigned cvt_pk_bf16(float lo, float hi) { unsigned r; asm volatile("v_cvt_pk_bf16_f32 %0, %1, %2" : "=v"(r) : "v"(lo), "v"(hi)); return r; }
; __device__ __forceinline__ unsigned pk4_fp8(float a, float b, float c, float d) { int w = __builtin_amdgcn_cvt_pk_fp8_f32(a, b, 0, false); w = __builtin_amdgcn_cvt_pk_fp8_f32(c, d, w, true); return (unsigned)w; }
; #define LAS __attribute__((address_space(3)))
; __global__ void __launch_bounds__(NTHR, 2) mk_fwd(Args args) {
;     ...
;                 for (int rr = 0; rr < 4; ++rr) {
;                     const int rl = wave * 4 + rr, row = row0 + rl; f32x4 v[4]; float ss = 0.f;
; #pragma unroll
;                     for (int j = 0; j < 2; ++j) { const u32x4 xb = xq[rr][j]; v[2 * j] = (f32x4){bflo(xb.x), bfhi(xb.x), bflo(xb.y), bfhi(xb.y)}; v[2 * j + 1] = (f32x4){bflo(xb.z), bfhi(xb.z), bflo(xb.w), bfhi(xb.w)}; }
; #pragma unroll
;                     for (int j = 0; j < 4; ++j) ss += (v[j].x * v[j].x + v[j].y * v[j].y) + (v[j].z * v[j].z + v[j].w * v[j].w);
;                     const float rstd = __builtin_amdgcn_rsqf(wave_sum(ss) * (1.0f / DM) + EPS);
;                     u32x4 h8, hiw[2], low[2];
; #pragma unroll
;                     for (int j = 0; j < 4; ++j) {
;                         const f32x4 h = (v[j] * rstd) * gm[j] + sv[j];
;                         h8[j] = pk4_fp8(h.x, h.y, h.z, h.w);
;                         const unsigned h0 = pg8::cvt_pk_bf16(h.x, h.y), h1 = pg8::cvt_pk_bf16(h.z, h.w);
;                         hiw[j >> 1][2 * (j & 1)] = h0; hiw[j >> 1][2 * (j & 1) + 1] = h1;
;                         low[j >> 1][2 * (j & 1)] = pg8::cvt_pk_bf16(h.x - bflo(h0), h.y - bfhi(h0)); low[j >> 1][2 * (j & 1) + 1] = pg8::cvt_pk_bf16(h.z - bflo(h1), h.w - bfhi(h1));
;                     }
;                     *(u32x4*)((unsigned char*)H + (size_t)row * DM + col) = h8;
; #pragma unroll
;                     for (int j = 0; j < 2; ++j) { *(LAS u32x4*)(Thi + rl * TP + col * 2 + 16 * j) = hiw[j]; *(LAS u32x4*)(Tlo + rl * TP + col * 2 + 16 * j) = low[j]; }
;                 }
	v_sub_f32_e32 v161, v166, v161
	v_sub_f32_e32 v162, v167, v162
	v_mov_b32_e32 v166, v184
	v_mov_b32_e32 v167, v186
	v_cvt_pk_bf16_f32 v165, v170, v171
	v_cvt_pk_bf16_f32 v168, v161, v162
	v_pk_mul_f32 v[166:167], v[120:121], v[166:167] op_sel_hi:[0,1]
	v_lshlrev_b32_e32 v161, 16, v165
	v_and_b32_e32 v162, 0xffff0000, v165
	v_mov_b32_e32 v186, v185
	v_cvt_pk_fp8_f32 v160, v170, v171 op_sel:[0,0,1]
	v_sub_f32_e32 v161, v170, v161
	v_sub_f32_e32 v162, v171, v162
	v_pk_fma_f32 v[170:171], v[166:167], v[142:143], v[110:111]
	v_pk_mul_f32 v[166:167], v[120:121], v[186:187] op_sel_hi:[0,1]
	v_cvt_pk_bf16_f32 v169, v161, v162
	v_mov_b32_e32 v161, v121
	v_pk_fma_f32 v[172:173], v[166:167], v[140:141], v[112:113]
	v_cvt_pk_bf16_f32 v166, v170, v171
	v_cvt_pk_fp8_f32 v161, v170, v171
	v_lshlrev_b32_e32 v162, 16, v166
	v_sub_f32_e32 v162, v170, v162
	v_and_b32_e32 v170, 0xffff0000, v166
	v_sub_f32_e32 v170, v171, v170
	v_cvt_pk_bf16_f32 v167, v172, v173
	v_cvt_pk_bf16_f32 v170, v162, v170
	v_cvt_pk_fp8_f32 v161, v172, v173 op_sel:[0,0,1]
	v_lshlrev_b32_e32 v162, 16, v167
	v_sub_f32_e32 v171, v172, v162
	v_and_b32_e32 v162, 0xffff0000, v167
	v_sub_f32_e32 v176, v173, v162
	v_pk_mul_f32 v[172:173], v[120:121], v[190:191] op_sel_hi:[0,1]
	v_pk_fma_f32 v[174:175], v[172:173], v[136:137], v[114:115]
	v_pk_mul_f32 v[172:173], v[120:121], v[192:193] op_sel_hi:[0,1]
	v_mov_b32_e32 v162, v121
	v_cvt_pk_bf16_f32 v171, v171, v176
	v_pk_fma_f32 v[178:179], v[172:173], v[134:135], v[116:117]
	v_cvt_pk_bf16_f32 v172, v174, v175
	v_cvt_pk_fp8_f32 v162, v174, v175
	v_lshlrev_b32_e32 v176, 16, v172
	v_sub_f32_e32 v174, v174, v176
	v_and_b32_e32 v176, 0xffff0000, v172
	v_cvt_pk_bf16_f32 v173, v178, v179
	v_sub_f32_e32 v175, v175, v176
	v_cvt_pk_bf16_f32 v176, v174, v175
	v_lshlrev_b32_e32 v174, 16, v173
	v_sub_f32_e32 v177, v178, v174
	v_and_b32_e32 v174, 0xffff0000, v173
	v_sub_f32_e32 v184, v179, v174
	v_pk_mul_f32 v[174:175], v[120:121], v[180:181] op_sel_hi:[0,1]
	v_cvt_pk_fp8_f32 v162, v178, v179 op_sel:[0,0,1]
	v_pk_fma_f32 v[178:179], v[174:175], v[138:139], v[106:107]
	v_pk_mul_f32 v[174:175], v[120:121], v[182:183] op_sel_hi:[0,1]
	v_cvt_pk_fp8_f32 v163, v178, v179
	v_cvt_pk_bf16_f32 v177, v177, v184
	v_pk_fma_f32 v[180:181], v[174:175], v[132:133], v[108:109]
	v_cvt_pk_bf16_f32 v174, v178, v179
	v_and_b32_e32 v191, 0xffff0000, v101
	v_lshlrev_b32_e32 v120, 16, v174
	v_cvt_pk_fp8_f32 v163, v180, v181 op_sel:[0,0,1]
	v_sub_f32_e32 v120, v178, v120
	v_and_b32_e32 v178, 0xffff0000, v174
	v_sub_f32_e32 v178, v179, v178
	v_cvt_pk_bf16_f32 v175, v180, v181
	v_cvt_pk_bf16_f32 v178, v120, v178
	v_and_b32_e32 v190, 0xffff0000, v100
	v_lshlrev_b32_e32 v120, 16, v175
	v_and_b32_e32 v179, 0xffff0000, v175
	v_sub_f32_e32 v120, v180, v120
	v_sub_f32_e32 v179, v181, v179
	v_lshl_add_u64 v[180:181], v[128:129], 0, s[44:45]
	v_cvt_pk_bf16_f32 v179, v120, v179
	global_store_dwordx4 v[180:181], v[160:163], off
	v_lshlrev_b32_e32 v181, 16, v96
	v_pk_mul_f32 v[192:193], v[190:191], v[190:191]
	v_and_b32_e32 v163, 0xffff0000, v99
	v_and_b32_e32 v161, 0xffff0000, v98
	v_lshlrev_b32_e32 v162, 16, v99
	v_mul_f32_e32 v120, v163, v163
	v_lshlrev_b32_e32 v160, 16, v98
	v_pk_fma_f32 v[186:187], v[162:163], v[162:163], v[120:121] op_sel_hi:[1,1,0]
	v_mul_f32_e32 v120, v161, v161
	v_pk_fma_f32 v[198:199], v[160:161], v[160:161], v[120:121] op_sel_hi:[1,1,0]
	v_and_b32_e32 v183, 0xffff0000, v96
	v_pk_fma_f32 v[192:193], v[188:189], v[188:189], v[192:193]
	v_mov_b32_e32 v180, v198
	v_mov_b32_e32 v200, v186
	v_mov_b32_e32 v201, v181
	v_mul_f32_e32 v182, v183, v183
	v_pk_add_f32 v[186:187], v[198:199], v[186:187]
	v_pk_mul_f32 v[198:199], v[180:181], v[200:201]
	v_pk_add_f32 v[192:193], v[192:193], v[192:193] op_sel:[0,1] op_sel_hi:[1,0]
	v_mov_b32_e32 v187, v199
	v_mov_b32_e32 v193, v182
	v_mul_f32_e32 v120, v195, v195
	v_lshlrev_b32_e32 v184, 16, v97
	v_and_b32_e32 v185, 0xffff0000, v97
	v_pk_add_f32 v[186:187], v[186:187], v[192:193]
	v_pk_fma_f32 v[192:193], v[194:195], v[194:195], v[120:121] op_sel_hi:[1,1,0]
	v_mul_f32_e32 v120, v197, v197
	v_mul_f32_e32 v203, v184, v184
	v_mul_f32_e32 v204, v185, v185
	v_pk_fma_f32 v[198:199], v[196:197], v[196:197], v[120:121] op_sel_hi:[1,1,0]
	v_mov_b32_e32 v193, v203
	v_mov_b32_e32 v199, v204
	v_pk_add_f32 v[192:193], v[192:193], v[198:199]
	ds_write_b128 v159, v[164:167] offset:2064
	ds_write_b128 v202, v[168:171] offset:2064
	ds_write_b128 v159, v[172:175] offset:2080
	v_pk_add_f32 v[186:187], v[186:187], v[192:193]
	ds_write_b128 v202, v[176:179] offset:2080
	v_add_f32_e32 v120, v186, v187
	v_mov_b32_e32 v182, v181
	s_nop 0
	v_add_f32_dpp v120, v120, v120 quad_perm:[1,0,3,2] row_mask:0xf bank_mask:0xf bound_ctrl:1
	s_nop 1
	v_add_f32_dpp v120, v120, v120 quad_perm:[2,3,0,1] row_mask:0xf bank_mask:0xf bound_ctrl:1
	s_nop 1
	v_add_f32_dpp v120, v120, v120 row_half_mirror row_mask:0xf bank_mask:0xf bound_ctrl:1
	s_nop 1
	v_add_f32_dpp v120, v120, v120 row_mirror row_mask:0xf bank_mask:0xf bound_ctrl:1
	s_nop 0
	v_readlane_b32 s17, v120, 16
	v_readlane_b32 s46, v120, 48
	v_readlane_b32 s44, v120, 0
	v_readlane_b32 s45, v120, 32
	v_mov_b32_e32 v186, s17
	v_mov_b32_e32 v187, s46
	v_pk_add_f32 v[186:187], s[44:45], v[186:187]
	s_ashr_i32 s17, s16, 31
	v_add_f32_e32 v120, v186, v187
	v_fmamk_f32 v120, v120, 0x3a800000, v154
	v_rsq_f32_e32 v120, v120
	s_lshl_b64 s[16:17], s[16:17], 10
	s_cmpk_gt_i32 s67, 0x87f
	s_cselect_b64 s[44:45], -1, 0
	v_pk_mul_f32 v[160:161], v[120:121], v[160:161] op_sel_hi:[0,1]
	v_pk_fma_f32 v[146:147], v[160:161], v[146:147], v[102:103]
	v_mov_b32_e32 v102, v121
	v_cvt_pk_fp8_f32 v102, v146, v147
; __device__ __forceinline__ unsigned cvt_pk_bf16(float lo, float hi) { unsigned r; asm volatile("v_cvt_pk_bf16_f32 %0, %1, %2" : "=v"(r) : "v"(lo), "v"(hi)); return r; }
; __device__ __forceinline__ unsigned pk4_fp8(float a, float b, float c, float d) { int w = __builtin_amdgcn_cvt_pk_fp8_f32(a, b, 0, false); w = __builtin_amdgcn_cvt_pk_fp8_f32(c, d, w, true); return (unsigned)w; }
; #define LAS __attribute__((address_space(3)))
; __global__ void __launch_bounds__(NTHR, 2) mk_fwd(Args args) {
;     ...
;                     for (int j = 0; j < 4; ++j) {
;                         const f32x4 h = (v[j] * rstd) * gm[j] + sv[j];
;                         h8[j] = pk4_fp8(h.x, h.y, h.z, h.w);
;                         const unsigned h0 = pg8::cvt_pk_bf16(h.x, h.y), h1 = pg8::cvt_pk_bf16(h.z, h.w);
;                         hiw[j >> 1][2 * (j & 1)] = h0; hiw[j >> 1][2 * (j & 1) + 1] = h1;
;                         low[j >> 1][2 * (j & 1)] = pg8::cvt_pk_bf16(h.x - bflo(h0), h.y - bfhi(h0)); low[j >> 1][2 * (j & 1) + 1] = pg8::cvt_pk_bf16(h.z - bflo(h1), h.w - bfhi(h1));
;                     }
;                     *(u32x4*)((unsigned char*)H + (size_t)row * DM + col) = h8;
; #pragma unroll
;                     for (int j = 0; j < 2; ++j) { *(LAS u32x4*)(Thi + rl * TP + col * 2 + 16 * j) = hiw[j]; *(LAS u32x4*)(Tlo + rl * TP + col * 2 + 16 * j) = low[j]; }
;                 }
;                 __syncthreads();
;                 if (grp + G < nmoe / 32) {
; #pragma unroll
;                     for (int rr = 0; rr < 4; ++rr)
; #pragma unroll
;                         for (int j = 0; j < 2; ++j) xq[rr][j] = *(const u32x4*)(X1 + (size_t)((grp + G) * 32 + wave * 4 + rr) * DM + lane * 16 + 8 * j);
;                 }
	v_pk_mul_f32 v[160:161], v[120:121], v[162:163] op_sel_hi:[0,1]
	v_pk_fma_f32 v[104:105], v[160:161], v[144:145], v[104:105]
	v_cvt_pk_bf16_f32 v144, v146, v147
	s_and_b64 vcc, exec, s[44:45]
	v_lshlrev_b32_e32 v103, 16, v144
	v_sub_f32_e32 v103, v146, v103
	v_and_b32_e32 v146, 0xffff0000, v144
	v_cvt_pk_bf16_f32 v145, v104, v105
	v_sub_f32_e32 v146, v147, v146
	v_cvt_pk_bf16_f32 v160, v103, v146
	v_lshlrev_b32_e32 v103, 16, v145
	v_cvt_pk_fp8_f32 v102, v104, v105 op_sel:[0,0,1]
	v_sub_f32_e32 v103, v104, v103
	v_and_b32_e32 v104, 0xffff0000, v145
	v_sub_f32_e32 v104, v105, v104
	v_cvt_pk_bf16_f32 v161, v103, v104
	v_mov_b32_e32 v104, v188
	v_mov_b32_e32 v105, v190
	v_pk_mul_f32 v[104:105], v[120:121], v[104:105] op_sel_hi:[0,1]
	v_pk_fma_f32 v[104:105], v[104:105], v[142:143], v[110:111]
	v_mov_b32_e32 v103, v121
	v_mov_b32_e32 v190, v189
	v_cvt_pk_fp8_f32 v103, v104, v105
	v_pk_mul_f32 v[110:111], v[120:121], v[190:191] op_sel_hi:[0,1]
	v_pk_fma_f32 v[110:111], v[110:111], v[140:141], v[112:113]
	v_cvt_pk_bf16_f32 v146, v104, v105
	s_nop 0
	v_lshlrev_b32_e32 v112, 16, v146
	v_sub_f32_e32 v104, v104, v112
	v_and_b32_e32 v112, 0xffff0000, v146
	v_cvt_pk_bf16_f32 v147, v110, v111
	v_sub_f32_e32 v105, v105, v112
	v_cvt_pk_bf16_f32 v162, v104, v105
	v_lshlrev_b32_e32 v104, 16, v147
	v_cvt_pk_fp8_f32 v103, v110, v111 op_sel:[0,0,1]
	v_sub_f32_e32 v110, v110, v104
	v_and_b32_e32 v104, 0xffff0000, v147
	v_sub_f32_e32 v111, v111, v104
	v_pk_mul_f32 v[104:105], v[120:121], v[194:195] op_sel_hi:[0,1]
	v_pk_fma_f32 v[112:113], v[104:105], v[136:137], v[114:115]
	v_mov_b32_e32 v104, v121
	v_cvt_pk_bf16_f32 v163, v110, v111
	v_pk_mul_f32 v[110:111], v[120:121], v[196:197] op_sel_hi:[0,1]
	v_cvt_pk_fp8_f32 v104, v112, v113
	v_pk_fma_f32 v[116:117], v[110:111], v[134:135], v[116:117]
	v_cvt_pk_bf16_f32 v110, v112, v113
	s_nop 0
	v_lshlrev_b32_e32 v105, 16, v110
	v_sub_f32_e32 v105, v112, v105
	v_and_b32_e32 v112, 0xffff0000, v110
	v_cvt_pk_bf16_f32 v111, v116, v117
	v_sub_f32_e32 v112, v113, v112
	v_cvt_pk_bf16_f32 v114, v105, v112
	v_lshlrev_b32_e32 v105, 16, v111
	v_sub_f32_e32 v115, v116, v105
	v_and_b32_e32 v105, 0xffff0000, v111
	v_pk_mul_f32 v[112:113], v[120:121], v[182:183] op_sel_hi:[0,1]
	v_cvt_pk_fp8_f32 v104, v116, v117 op_sel:[0,0,1]
	v_sub_f32_e32 v116, v117, v105
	v_pk_fma_f32 v[106:107], v[112:113], v[138:139], v[106:107]
	v_mov_b32_e32 v105, v121
	v_cvt_pk_fp8_f32 v105, v106, v107
	v_pk_mul_f32 v[112:113], v[120:121], v[184:185] op_sel_hi:[0,1]
	v_cvt_pk_bf16_f32 v115, v115, v116
	v_pk_fma_f32 v[108:109], v[112:113], v[132:133], v[108:109]
	v_cvt_pk_bf16_f32 v112, v106, v107
	s_nop 0
	v_lshlrev_b32_e32 v116, 16, v112
	v_sub_f32_e32 v106, v106, v116
	v_and_b32_e32 v116, 0xffff0000, v112
	v_cvt_pk_fp8_f32 v105, v108, v109 op_sel:[0,0,1]
	v_sub_f32_e32 v107, v107, v116
	v_cvt_pk_bf16_f32 v113, v108, v109
	v_cvt_pk_bf16_f32 v116, v106, v107
	s_nop 0
	v_lshlrev_b32_e32 v106, 16, v113
	v_and_b32_e32 v107, 0xffff0000, v113
	v_sub_f32_e32 v106, v108, v106
	v_sub_f32_e32 v107, v109, v107
	v_cvt_pk_bf16_f32 v117, v106, v107
	v_lshl_add_u64 v[106:107], v[128:129], 0, s[16:17]
	global_store_dwordx4 v[106:107], v[102:105], off
	ds_write_b128 v159, v[144:147] offset:4128
	ds_write_b128 v202, v[160:163] offset:4128
	ds_write_b128 v159, v[110:113] offset:4144
	ds_write_b128 v202, v[114:117] offset:4144
	s_waitcnt lgkmcnt(0)
	s_barrier
	global_load_dwordx4 v[176:179], v[122:123], off offset:768
	global_load_dwordx4 v[180:183], v[122:123], off offset:832
	global_load_dwordx4 v[184:187], v[122:123], off offset:896
	global_load_dwordx4 v[188:191], v[122:123], off offset:960
	s_add_i32 s16, s56, s61
	s_ashr_i32 s17, s16, 31
	s_lshl_b64 s[46:47], s[16:17], 11
	v_lshl_add_u64 v[74:75], v[130:131], 0, s[46:47]
	s_add_i32 s46, s16, 1
	s_ashr_i32 s47, s46, 31
	s_lshl_b64 s[46:47], s[46:47], 11
	v_lshl_add_u64 v[82:83], v[130:131], 0, s[46:47]
	s_add_i32 s46, s16, 2
	s_add_i32 s16, s16, 3
	s_ashr_i32 s47, s46, 31
	s_ashr_i32 s17, s16, 31
	s_lshl_b64 s[46:47], s[46:47], 11
	s_lshl_b64 s[16:17], s[16:17], 11
	v_lshl_add_u64 v[90:91], v[130:131], 0, s[46:47]
	v_lshl_add_u64 v[98:99], v[130:131], 0, s[16:17]
	global_load_dwordx4 v[70:73], v[74:75], off offset:16
	s_nop 0
	global_load_dwordx4 v[74:77], v[74:75], off
	s_nop 0
	global_load_dwordx4 v[78:81], v[82:83], off offset:16
	s_nop 0
	global_load_dwordx4 v[82:85], v[82:83], off
	s_nop 0
	global_load_dwordx4 v[86:89], v[90:91], off offset:16
	s_nop 0
	global_load_dwordx4 v[90:93], v[90:91], off
	s_nop 0
	global_load_dwordx4 v[94:97], v[98:99], off offset:16
	s_nop 0
	global_load_dwordx4 v[98:101], v[98:99], off
; #define LAS __attribute__((address_space(3)))
; __global__ void __launch_bounds__(NTHR, 2) mk_fwd(Args args) {
;     ...
;                 f32x4 acc = (f32x4){0.f, 0.f, 0.f, 0.f};
; #pragma unroll
;                 for (int st = 0; st < 16; ++st) {
;                     const int kb = (kh * 512 + 32 * st + 8 * q4) * 2;
;                     const fa::bf16x8 bh = *(const LAS fa::bf16x8*)(Thi + (rh * 16 + n16) * TP + kb), bl = *(const LAS fa::bf16x8*)(Tlo + (rh * 16 + n16) * TP + kb);
;                     acc = __builtin_amdgcn_mfma_f32_16x16x32_bf16(ah[st], bh, acc, 0, 0, 0);
;                     acc = __builtin_amdgcn_mfma_f32_16x16x32_bf16(ah[st], bl, acc, 0, 0, 0);
;                     acc = __builtin_amdgcn_mfma_f32_16x16x32_bf16(*(const fa::bf16x8*)(alp + 32 * st), bh, acc, 0, 0, 0);
;                 }
;                 if (kh == 1) *(LAS f32x4*)(PART + (wave & 3) * 1024 + lane * 16) = acc;
.LBB0_665:
	s_nop 0
	s_andn2_b64 vcc, exec, s[26:27]
	ds_read_b128 v[106:109], v155
	ds_read_b128 v[132:135], v156
	ds_read_b128 v[110:113], v155 offset:64
	ds_read_b128 v[136:139], v156 offset:64
	ds_read_b128 v[114:117], v155 offset:128
	ds_read_b128 v[140:143], v156 offset:128
	s_waitcnt lgkmcnt(5)
	v_mfma_f32_16x16x32_bf16 v[102:105], v[58:61], v[106:109], 0
	s_waitcnt lgkmcnt(4)
	v_mfma_f32_16x16x32_bf16 v[102:105], v[58:61], v[132:135], v[102:105]
	v_mfma_f32_16x16x32_bf16 v[102:105], v[206:209], v[106:109], v[102:105]
	ds_read_b128 v[106:109], v155 offset:192
	ds_read_b128 v[132:135], v156 offset:192
	s_waitcnt lgkmcnt(5)
	v_mfma_f32_16x16x32_bf16 v[102:105], v[2:5], v[110:113], v[102:105]
	s_waitcnt lgkmcnt(4)
	v_mfma_f32_16x16x32_bf16 v[102:105], v[2:5], v[136:139], v[102:105]
	v_mfma_f32_16x16x32_bf16 v[102:105], v[210:213], v[110:113], v[102:105]
	ds_read_b128 v[110:113], v155 offset:256
	ds_read_b128 v[136:139], v156 offset:256
	s_waitcnt lgkmcnt(5)
	v_mfma_f32_16x16x32_bf16 v[102:105], v[6:9], v[114:117], v[102:105]
	s_waitcnt lgkmcnt(4)
	v_mfma_f32_16x16x32_bf16 v[102:105], v[6:9], v[140:143], v[102:105]
	v_mfma_f32_16x16x32_bf16 v[102:105], v[214:217], v[114:117], v[102:105]
	ds_read_b128 v[114:117], v155 offset:320
	ds_read_b128 v[140:143], v156 offset:320
	s_waitcnt lgkmcnt(5)
	v_mfma_f32_16x16x32_bf16 v[102:105], v[10:13], v[106:109], v[102:105]
	s_waitcnt lgkmcnt(4)
	v_mfma_f32_16x16x32_bf16 v[102:105], v[10:13], v[132:135], v[102:105]
	v_mfma_f32_16x16x32_bf16 v[102:105], v[218:221], v[106:109], v[102:105]
	ds_read_b128 v[106:109], v155 offset:384
	ds_read_b128 v[132:135], v156 offset:384
	s_waitcnt lgkmcnt(5)
	v_mfma_f32_16x16x32_bf16 v[102:105], v[14:17], v[110:113], v[102:105]
	s_waitcnt lgkmcnt(4)
	v_mfma_f32_16x16x32_bf16 v[102:105], v[14:17], v[136:139], v[102:105]
	v_mfma_f32_16x16x32_bf16 v[102:105], v[222:225], v[110:113], v[102:105]
	ds_read_b128 v[110:113], v155 offset:448
	ds_read_b128 v[136:139], v156 offset:448
	s_waitcnt lgkmcnt(5)
	v_mfma_f32_16x16x32_bf16 v[102:105], v[18:21], v[114:117], v[102:105]
	s_waitcnt lgkmcnt(4)
	v_mfma_f32_16x16x32_bf16 v[102:105], v[18:21], v[140:143], v[102:105]
	v_mfma_f32_16x16x32_bf16 v[102:105], v[226:229], v[114:117], v[102:105]
	ds_read_b128 v[114:117], v155 offset:512
	ds_read_b128 v[140:143], v156 offset:512
	s_waitcnt lgkmcnt(5)
	v_mfma_f32_16x16x32_bf16 v[102:105], v[22:25], v[106:109], v[102:105]
	s_waitcnt lgkmcnt(4)
	v_mfma_f32_16x16x32_bf16 v[102:105], v[22:25], v[132:135], v[102:105]
	v_mfma_f32_16x16x32_bf16 v[102:105], v[230:233], v[106:109], v[102:105]
	ds_read_b128 v[106:109], v155 offset:576
	ds_read_b128 v[132:135], v156 offset:576
	s_waitcnt lgkmcnt(5)
	v_mfma_f32_16x16x32_bf16 v[102:105], v[26:29], v[110:113], v[102:105]
	s_waitcnt lgkmcnt(4)
	v_mfma_f32_16x16x32_bf16 v[102:105], v[26:29], v[136:139], v[102:105]
	v_mfma_f32_16x16x32_bf16 v[102:105], v[234:237], v[110:113], v[102:105]
	ds_read_b128 v[110:113], v155 offset:640
	ds_read_b128 v[136:139], v156 offset:640
	s_waitcnt lgkmcnt(5)
	v_mfma_f32_16x16x32_bf16 v[102:105], v[30:33], v[114:117], v[102:105]
	s_waitcnt lgkmcnt(4)
	v_mfma_f32_16x16x32_bf16 v[102:105], v[30:33], v[140:143], v[102:105]
	v_mfma_f32_16x16x32_bf16 v[102:105], v[238:241], v[114:117], v[102:105]
	ds_read_b128 v[114:117], v155 offset:704
	ds_read_b128 v[140:143], v156 offset:704
	s_waitcnt lgkmcnt(5)
	v_mfma_f32_16x16x32_bf16 v[102:105], v[34:37], v[106:109], v[102:105]
	s_waitcnt lgkmcnt(4)
	v_mfma_f32_16x16x32_bf16 v[102:105], v[34:37], v[132:135], v[102:105]
	v_mfma_f32_16x16x32_bf16 v[102:105], v[242:245], v[106:109], v[102:105]
	ds_read_b128 v[106:109], v155 offset:768
	ds_read_b128 v[132:135], v156 offset:768
	s_waitcnt lgkmcnt(5)
	v_mfma_f32_16x16x32_bf16 v[102:105], v[38:41], v[110:113], v[102:105]
	s_waitcnt lgkmcnt(4)
	v_mfma_f32_16x16x32_bf16 v[102:105], v[38:41], v[136:139], v[102:105]
	v_mfma_f32_16x16x32_bf16 v[102:105], v[246:249], v[110:113], v[102:105]
	ds_read_b128 v[110:113], v155 offset:832
	ds_read_b128 v[136:139], v156 offset:832
	s_waitcnt lgkmcnt(5)
	v_mfma_f32_16x16x32_bf16 v[102:105], v[42:45], v[114:117], v[102:105]
	s_waitcnt lgkmcnt(4)
	v_mfma_f32_16x16x32_bf16 v[102:105], v[42:45], v[140:143], v[102:105]
	v_mfma_f32_16x16x32_bf16 v[102:105], v[250:253], v[114:117], v[102:105]
	ds_read_b128 v[114:117], v155 offset:896
	ds_read_b128 v[140:143], v156 offset:896
	s_waitcnt lgkmcnt(5)
	v_mfma_f32_16x16x32_bf16 v[102:105], v[46:49], v[106:109], v[102:105]
	s_waitcnt lgkmcnt(4)
	v_mfma_f32_16x16x32_bf16 v[102:105], v[46:49], v[132:135], v[102:105]
	s_waitcnt vmcnt(11)
	v_mfma_f32_16x16x32_bf16 v[102:105], v[176:179], v[106:109], v[102:105]
	ds_read_b128 v[106:109], v155 offset:960
	ds_read_b128 v[132:135], v156 offset:960
	s_waitcnt lgkmcnt(5)
	v_mfma_f32_16x16x32_bf16 v[102:105], v[50:53], v[110:113], v[102:105]
	s_waitcnt lgkmcnt(4)
	v_mfma_f32_16x16x32_bf16 v[102:105], v[50:53], v[136:139], v[102:105]
	s_waitcnt vmcnt(10)
	v_mfma_f32_16x16x32_bf16 v[102:105], v[180:183], v[110:113], v[102:105]
	s_waitcnt lgkmcnt(3)
	v_mfma_f32_16x16x32_bf16 v[102:105], v[54:57], v[114:117], v[102:105]
	s_waitcnt lgkmcnt(2)
	v_mfma_f32_16x16x32_bf16 v[102:105], v[54:57], v[140:143], v[102:105]
	s_waitcnt vmcnt(9)
	v_mfma_f32_16x16x32_bf16 v[102:105], v[184:187], v[114:117], v[102:105]
	s_waitcnt lgkmcnt(1)
	v_mfma_f32_16x16x32_bf16 v[102:105], v[62:65], v[106:109], v[102:105]
	s_waitcnt lgkmcnt(0)
	v_mfma_f32_16x16x32_bf16 v[102:105], v[62:65], v[132:135], v[102:105]
	s_waitcnt vmcnt(8)
	v_mfma_f32_16x16x32_bf16 v[102:105], v[188:191], v[106:109], v[102:105]
	s_cbranch_vccnz .LBB0_667
	v_add_u32_e32 v106, s57, v124
	s_nop 5
	ds_write_b128 v106, v[102:105]

; #define LAS __attribute__((address_space(3)))
; __global__ void __launch_bounds__(NTHR, 2) mk_fwd(Args args) {
;     ...
;             const bf16* wrt_hi = WSP(bf16, WS_WRT) + (size_t)l * 65536; const bf16* wrt_lo = wrt_hi + 32768;
;             const float* br = router_b + l * NEXP; const float* g = norm2_g + l * DM;
;             constexpr int TP = 2064;
;             LAS unsigned char* Thi = lds; LAS unsigned char* Tlo = lds + 32 * TP; LAS unsigned char* PART = lds + 64 * TP; LAS float* LOG = (LAS float*)(lds + 64 * TP + 4096);
;             static_assert(64 * TP + 8192 <= LDS_CTL, "router LDS map");
;             const int eh = wave & 1, rh = (wave >> 1) & 1, kh = wave >> 2, n16 = lane & 15, q4 = lane >> 4;
;             fa::bf16x8 ah[16];
; #pragma unroll
;             for (int st = 0; st < 16; ++st) { const int k = kh * 512 + 32 * st + 8 * q4;
;                 ah[st] = *(const fa::bf16x8*)(wrt_hi + (eh * 16 + n16) * DM + k); }
;             const bf16* alp = wrt_lo + (eh * 16 + n16) * DM + kh * 512 + 8 * q4;
;             const f32x4 brv = *(const f32x4*)(br + eh * 16 + 4 * q4);
;             if (tid < 32) lctl[tid] = 0;
;             __syncthreads();
;             u32x4 xq[4][2];
;             if (bx < nmoe / 32) {
; #pragma unroll
;                 for (int rr = 0; rr < 4; ++rr)
; #pragma unroll
;                     for (int j = 0; j < 2; ++j) xq[rr][j] = *(const u32x4*)(X1 + (size_t)(bx * 32 + wave * 4 + rr) * DM + lane * 16 + 8 * j);
;             }
;             for (int grp = bx; grp < nmoe / 32; grp += G) {
.LBB0_1565:
	s_andn2_b64 vcc, exec, s[12:13]
	s_cbranch_vccnz .LBB0_1608
	s_lshl_b32 s12, s7, 4
	s_add_u32 s20, s18, 0x33c00000
	s_load_dwordx2 s[8:9], s[8:9], 0x38
	s_addc_u32 s21, s19, 0
	v_or_b32_e32 v105, s12, v118
	s_add_u32 s22, s18, 0x33a00000
	v_lshlrev_b32_e32 v120, 11, v105
	v_mov_b32_e32 v121, 0
	s_addc_u32 s23, s19, 0
	v_lshl_add_u64 v[108:109], s[18:19], 0, v[120:121]
	s_ashr_i32 s7, s6, 31
	v_lshl_add_u64 v[108:109], s[6:7], 1, v[108:109]
	v_lshlrev_b32_e32 v120, 1, v107
	v_lshl_add_u64 v[108:109], v[108:109], 0, v[120:121]
	s_mov_b64 s[6:7], 0x340000
	v_lshlrev_b32_e32 v120, 6, v103
	v_lshl_add_u64 v[122:123], v[108:109], 0, s[6:7]
	v_lshlrev_b32_e32 v124, 4, v103
	v_mov_b32_e32 v125, v121
	s_waitcnt lgkmcnt(0)
	v_lshl_add_u64 v[108:109], s[8:9], 0, v[120:121]
	s_mov_b64 s[6:7], 0x1000
	v_lshl_add_u64 v[126:127], v[108:109], 0, s[6:7]
	v_lshl_add_u64 v[108:109], s[18:19], 0, v[124:125]
	s_mov_b64 s[6:7], 0x19200000
	s_lshl_b32 s54, s57, 2
	v_lshl_add_u64 v[128:129], v[108:109], 0, s[6:7]
	s_add_i32 s6, 0, 0x10200
	s_lshr_b32 s7, s14, 3
	v_mov_b32_e32 v105, v121
	s_cmp_eq_u32 s15, 1
	v_add_u32_e32 v148, s6, v104
	v_lshl_add_u64 v[130:131], s[10:11], 0, v[104:105]
	v_and_or_b32 v103, s7, 16, v118
	s_movk_i32 s7, 0x810
	v_mov_b32_e32 v105, s6
	s_cselect_b64 s[24:25], -1, 0
	s_lshl_b32 s6, s57, 10
	v_add_u32_e32 v125, 0, v104
	v_mad_u32_u24 v104, v103, s7, 0
	v_mad_u32_u24 v103, v103, s7, v105
	s_and_b32 s7, s6, 0xc00
	s_add_i32 s56, 0, 0x20400
	s_add_i32 s55, s56, s7
	s_cmpk_lt_u32 s14, 0x100
	s_cselect_b64 s[26:27], -1, 0
	s_lshl_b32 s7, s14, 4
	s_and_b32 s7, s7, 0xfffff800
	s_add_i32 s8, 0, 0x21400
	v_lshlrev_b32_e32 v110, 2, v106
	s_add_i32 s7, s8, s7
	s_lshl_b32 s9, s12, 2
	v_lshlrev_b32_e32 v105, 7, v118
	s_add_i32 s9, s9, s7
	v_lshlrev_b32_e32 v107, 2, v110
	v_add3_u32 v149, s9, v105, v107
	v_or_b32_e32 v105, s54, v106
	v_lshlrev_b32_e32 v105, 7, v105
	v_lshlrev_b32_e32 v150, 1, v118
	v_lshlrev_b32_e32 v107, 3, v118
	s_or_b32 s58, s54, 1
	v_lshlrev_b32_e32 v102, 1, v102
	s_add_i32 s14, s2, s64
	s_lshl_b32 s61, s2, 5
	s_add_i32 s56, s56, s6
	v_add3_u32 v151, s8, v105, v107
	v_or_b32_e32 v152, 1, v150
	v_cmp_gt_u32_e64 s[6:7], 4, v118
	v_cmp_eq_u32_e64 s[8:9], 0, v118
	v_cmp_eq_u32_e64 s[10:11], 1, v118
	v_cmp_eq_u32_e64 s[12:13], 2, v118
	s_mulk_i32 s57, 0x2040
	s_mulk_i32 s58, 0x810
	s_lshl_b32 s59, s14, 5
	s_lshl_b32 s60, s64, 5
	v_or_b32_e32 v153, s61, v106
	s_mov_b64 s[28:29], 0x16a000
	s_mov_b64 s[30:31], 0x169000
	s_mov_b32 s62, 0x16a000
	s_mov_b32 s63, 0x169000
	v_mov_b32_e32 v154, 0x358637bd
	v_add_u32_e32 v155, v104, v102
	v_add_u32_e32 v156, v103, v102
	v_mov_b32_e32 v157, 1
	v_mov_b32_e32 v158, 0xff61b1e6
	s_mov_b32 s65, s2
	global_load_dwordx4 v[206:209], v[122:123], off
	global_load_dwordx4 v[210:213], v[122:123], off offset:64
	global_load_dwordx4 v[214:217], v[122:123], off offset:128
	global_load_dwordx4 v[218:221], v[122:123], off offset:192
	global_load_dwordx4 v[222:225], v[122:123], off offset:256
	global_load_dwordx4 v[226:229], v[122:123], off offset:320
	global_load_dwordx4 v[230:233], v[122:123], off offset:384
	global_load_dwordx4 v[234:237], v[122:123], off offset:448
	global_load_dwordx4 v[238:241], v[122:123], off offset:512
	global_load_dwordx4 v[242:245], v[122:123], off offset:576
	global_load_dwordx4 v[246:249], v[122:123], off offset:640
	global_load_dwordx4 v[250:253], v[122:123], off offset:704
	s_branch .LBB0_1568

; __global__ void __launch_bounds__(NTHR, 2) mk_fwd(Args args) {
;     ...
;             for (int grp = bx; grp < nmoe / 32; grp += G) {
;                 const int row0 = grp * 32; const int b = row0 < TL ? (row0 >> 12) : 16;
;                 const float* sh = modl + (size_t)b * (NMOD * DM) + 3 * DM; const float* sc = sh + DM;
;                 const int col = lane * 16;
;                 f32x4 gm[4], sv[4];
; #pragma unroll
;                 for (int j = 0; j < 4; ++j) { gm[j] = *(const f32x4*)(g + col + 4 * j) * (*(const f32x4*)(sc + col + 4 * j) + 1.0f); sv[j] = *(const f32x4*)(sh + col + 4 * j); }
; #pragma unroll
;                 for (int rr = 0; rr < 4; ++rr) {
;                     const int rl = wave * 4 + rr, row = row0 + rl; f32x4 v[4]; float ss = 0.f;
; #pragma unroll
;                     for (int j = 0; j < 2; ++j) { const u32x4 xb = xq[rr][j]; v[2 * j] = (f32x4){bflo(xb.x), bfhi(xb.x), bflo(xb.y), bfhi(xb.y)}; v[2 * j + 1] = (f32x4){bflo(xb.z), bfhi(xb.z), bflo(xb.w), bfhi(xb.w)}; }
; #pragma unroll
;                     for (int j = 0; j < 4; ++j) ss += (v[j].x * v[j].x + v[j].y * v[j].y) + (v[j].z * v[j].z + v[j].w * v[j].w);
;                     const float rstd = __builtin_amdgcn_rsqf(wave_sum(ss) * (1.0f / DM) + EPS);
.LBB0_1568:
	s_ashr_i32 s14, s65, 7
	s_mul_hi_i32 s15, s14, 0x6000
	s_mulk_i32 s14, 0x6000
	s_add_u32 s14, s18, s14
	s_addc_u32 s15, s19, s15
	v_lshlrev_b32_e32 v120, 2, v124
	v_lshl_add_u64 v[106:107], s[14:15], 0, v[120:121]
	v_add_co_u32_e32 v102, vcc, s62, v106
	v_lshl_add_u64 v[116:117], v[106:107], 0, s[30:31]
	s_nop 0
	v_addc_co_u32_e32 v103, vcc, 0, v107, vcc
	global_load_dwordx4 v[132:135], v[102:103], off
	v_lshl_add_u64 v[102:103], v[106:107], 0, s[28:29]
	global_load_dwordx4 v[136:139], v[102:103], off offset:16
	global_load_dwordx4 v[140:143], v[102:103], off offset:32
	global_load_dwordx4 v[160:163], v[126:127], off
	global_load_dwordx4 v[164:167], v[126:127], off offset:16
	global_load_dwordx4 v[168:171], v[126:127], off offset:32
	global_load_dwordx4 v[172:175], v[126:127], off offset:48
	global_load_dwordx4 v[176:179], v[102:103], off offset:48
	v_add_co_u32_e32 v102, vcc, s63, v106
	global_load_dwordx4 v[110:113], v[116:117], off offset:16
	s_nop 0
	v_addc_co_u32_e32 v103, vcc, 0, v107, vcc
	global_load_dwordx4 v[102:105], v[102:103], off
	s_waitcnt vmcnt(16)
	v_and_b32_e32 v187, 0xffff0000, v74
	v_and_b32_e32 v189, 0xffff0000, v75
	v_and_b32_e32 v193, 0xffff0000, v77
	v_and_b32_e32 v192, 0xffff0000, v76
	v_lshlrev_b32_e32 v181, 16, v72
	v_lshlrev_b32_e32 v186, 16, v74
	v_lshlrev_b32_e32 v188, 16, v75
	v_lshlrev_b32_e32 v191, 16, v77
	v_lshlrev_b32_e32 v190, 16, v76
	v_and_b32_e32 v197, 0xffff0000, v71
	v_mul_f32_e32 v108, v189, v189
	v_pk_mul_f32 v[114:115], v[192:193], v[192:193]
	v_mul_f32_e32 v106, v187, v187
	v_lshlrev_b32_e32 v196, 16, v71
	v_mov_b32_e32 v145, v181
	v_mul_f32_e32 v144, v197, v197
	v_pk_fma_f32 v[108:109], v[188:189], v[188:189], v[108:109] op_sel_hi:[1,1,0]
	v_pk_fma_f32 v[114:115], v[190:191], v[190:191], v[114:115]
	v_pk_fma_f32 v[106:107], v[186:187], v[186:187], v[106:107] op_sel_hi:[1,1,0]
	v_pk_fma_f32 v[198:199], v[196:197], v[196:197], v[144:145] op_sel_hi:[1,1,0]
	v_mov_b32_e32 v180, v106
	v_mov_b32_e32 v144, v108
	v_pk_add_f32 v[200:201], v[106:107], v[108:109]
	v_pk_add_f32 v[202:203], v[114:115], v[114:115] op_sel:[0,1] op_sel_hi:[1,0]
	global_load_dwordx4 v[106:109], v[116:117], off offset:48
	s_nop 0
	global_load_dwordx4 v[114:117], v[116:117], off offset:32
	v_and_b32_e32 v195, 0xffff0000, v70
	v_and_b32_e32 v183, 0xffff0000, v72
	v_lshlrev_b32_e32 v184, 16, v73
	v_and_b32_e32 v185, 0xffff0000, v73
	v_lshlrev_b32_e32 v194, 16, v70
	v_mul_f32_e32 v120, v195, v195
	v_mul_f32_e32 v159, v183, v183
	v_mul_f32_e32 v182, v184, v184
	v_mul_f32_e32 v204, v185, v185
	v_pk_fma_f32 v[146:147], v[194:195], v[194:195], v[120:121] op_sel_hi:[1,1,0]
	v_pk_mul_f32 v[144:145], v[180:181], v[144:145]
	v_mov_b32_e32 v147, v182
	v_mov_b32_e32 v199, v204
	v_mov_b32_e32 v203, v159
	v_mov_b32_e32 v201, v145
	v_pk_add_f32 v[146:147], v[146:147], v[198:199]
	v_pk_add_f32 v[144:145], v[200:201], v[202:203]
	v_mov_b32_e32 v182, v181
	v_pk_add_f32 v[144:145], v[144:145], v[146:147]
	v_add_u32_e32 v202, s58, v148
	v_add_f32_e32 v120, v144, v145
	s_add_i32 s65, s65, s64
	s_waitcnt vmcnt(10)
	v_pk_add_f32 v[136:137], v[136:137], 1.0 op_sel_hi:[1,0]
	v_add_f32_dpp v120, v120, v120 quad_perm:[1,0,3,2] row_mask:0xf bank_mask:0xf bound_ctrl:1
	v_pk_add_f32 v[138:139], v[138:139], 1.0 op_sel_hi:[1,0]
	s_waitcnt vmcnt(9)
	v_pk_add_f32 v[198:199], v[142:143], 1.0 op_sel_hi:[1,0]
	v_add_f32_dpp v120, v120, v120 quad_perm:[2,3,0,1] row_mask:0xf bank_mask:0xf bound_ctrl:1
	v_pk_add_f32 v[132:133], v[132:133], 1.0 op_sel_hi:[1,0]
	v_pk_add_f32 v[134:135], v[134:135], 1.0 op_sel_hi:[1,0]
	v_add_f32_dpp v120, v120, v120 row_half_mirror row_mask:0xf bank_mask:0xf bound_ctrl:1
	s_waitcnt vmcnt(8)
	v_pk_mul_f32 v[146:147], v[160:161], v[132:133]
	v_pk_mul_f32 v[144:145], v[162:163], v[134:135]
	v_add_f32_dpp v120, v120, v120 row_mirror row_mask:0xf bank_mask:0xf bound_ctrl:1
	s_waitcnt vmcnt(7)
	v_pk_mul_f32 v[142:143], v[164:165], v[136:137]
	v_readlane_b32 s34, v120, 16
	v_readlane_b32 s35, v120, 48
	v_readlane_b32 s14, v120, 0
	v_readlane_b32 s15, v120, 32
	v_mov_b32_e32 v132, s34
	v_mov_b32_e32 v133, s35
	v_pk_add_f32 v[132:133], s[14:15], v[132:133]
	v_pk_add_f32 v[200:201], v[140:141], 1.0 op_sel_hi:[1,0]
	v_add_f32_e32 v120, v132, v133
	v_fmamk_f32 v120, v120, 0x3a800000, v154
	v_rsq_f32_e32 v120, v120
	v_pk_mul_f32 v[140:141], v[166:167], v[138:139]
	s_waitcnt vmcnt(6)
	v_pk_mul_f32 v[136:137], v[168:169], v[200:201]
	s_waitcnt vmcnt(4)
	v_pk_add_f32 v[138:139], v[176:177], 1.0 op_sel_hi:[1,0]
	v_pk_mul_f32 v[160:161], v[120:121], v[186:187] op_sel_hi:[0,1]
	s_waitcnt vmcnt(2)
	v_pk_fma_f32 v[162:163], v[160:161], v[146:147], v[102:103]
	v_mov_b32_e32 v160, v121
	v_cvt_pk_fp8_f32 v160, v162, v163
	v_pk_mul_f32 v[164:165], v[120:121], v[188:189] op_sel_hi:[0,1]
	v_pk_fma_f32 v[166:167], v[164:165], v[144:145], v[104:105]
	v_cvt_pk_bf16_f32 v164, v162, v163
	v_pk_mul_f32 v[138:139], v[172:173], v[138:139]
	v_lshlrev_b32_e32 v159, 16, v164
	v_and_b32_e32 v161, 0xffff0000, v164
	v_sub_f32_e32 v159, v162, v159
	v_sub_f32_e32 v161, v163, v161
	v_cvt_pk_bf16_f32 v165, v166, v167
	v_cvt_pk_bf16_f32 v168, v159, v161
	v_mov_b32_e32 v162, v190
	v_lshlrev_b32_e32 v159, 16, v165
	v_and_b32_e32 v161, 0xffff0000, v165
	v_mov_b32_e32 v163, v192
	v_mov_b32_e32 v192, v191
	v_cvt_pk_fp8_f32 v160, v166, v167 op_sel:[0,0,1]
	v_sub_f32_e32 v159, v166, v159
	v_sub_f32_e32 v161, v167, v161
	v_pk_mul_f32 v[162:163], v[120:121], v[162:163] op_sel_hi:[0,1]
	v_pk_mul_f32 v[166:167], v[120:121], v[192:193] op_sel_hi:[0,1]
	v_cvt_pk_bf16_f32 v169, v159, v161
	v_pk_fma_f32 v[162:163], v[162:163], v[142:143], v[110:111]
	v_mov_b32_e32 v161, v121
	v_pk_fma_f32 v[172:173], v[166:167], v[140:141], v[112:113]
	v_cvt_pk_bf16_f32 v166, v162, v163
	v_cvt_pk_fp8_f32 v161, v162, v163
	v_lshlrev_b32_e32 v159, 16, v166
	v_sub_f32_e32 v159, v162, v159
	v_and_b32_e32 v162, 0xffff0000, v166
	v_sub_f32_e32 v162, v163, v162
	v_pk_mul_f32 v[134:135], v[170:171], v[198:199]
	v_cvt_pk_bf16_f32 v167, v172, v173
	v_cvt_pk_bf16_f32 v170, v159, v162
	v_pk_add_f32 v[132:133], v[178:179], 1.0 op_sel_hi:[1,0]
	v_and_b32_e32 v162, 0xffff0000, v167
	v_sub_f32_e32 v171, v173, v162
	v_pk_mul_f32 v[162:163], v[120:121], v[194:195] op_sel_hi:[0,1]
	v_pk_mul_f32 v[132:133], v[174:175], v[132:133]
	v_lshlrev_b32_e32 v159, 16, v167
	s_waitcnt vmcnt(0)
; __device__ __forceinline__ unsigned cvt_pk_bf16(float lo, float hi) { unsigned r; asm volatile("v_cvt_pk_bf16_f32 %0, %1, %2" : "=v"(r) : "v"(lo), "v"(hi)); return r; }
; __device__ __forceinline__ unsigned pk4_fp8(float a, float b, float c, float d) { int w = __builtin_amdgcn_cvt_pk_fp8_f32(a, b, 0, false); w = __builtin_amdgcn_cvt_pk_fp8_f32(c, d, w, true); return (unsigned)w; }
; #define LAS __attribute__((address_space(3)))
; __global__ void __launch_bounds__(NTHR, 2) mk_fwd(Args args) {
;     ...
;                 for (int rr = 0; rr < 4; ++rr) {
;                     const int rl = wave * 4 + rr, row = row0 + rl; f32x4 v[4]; float ss = 0.f;
; #pragma unroll
;                     for (int j = 0; j < 2; ++j) { const u32x4 xb = xq[rr][j]; v[2 * j] = (f32x4){bflo(xb.x), bfhi(xb.x), bflo(xb.y), bfhi(xb.y)}; v[2 * j + 1] = (f32x4){bflo(xb.z), bfhi(xb.z), bflo(xb.w), bfhi(xb.w)}; }
; #pragma unroll
;                     for (int j = 0; j < 4; ++j) ss += (v[j].x * v[j].x + v[j].y * v[j].y) + (v[j].z * v[j].z + v[j].w * v[j].w);
;                     const float rstd = __builtin_amdgcn_rsqf(wave_sum(ss) * (1.0f / DM) + EPS);
;                     u32x4 h8, hiw[2], low[2];
; #pragma unroll
;                     for (int j = 0; j < 4; ++j) {
;                         const f32x4 h = (v[j] * rstd) * gm[j] + sv[j];
;                         h8[j] = pk4_fp8(h.x, h.y, h.z, h.w);
;                         const unsigned h0 = pg8::cvt_pk_bf16(h.x, h.y), h1 = pg8::cvt_pk_bf16(h.z, h.w);
;                         hiw[j >> 1][2 * (j & 1)] = h0; hiw[j >> 1][2 * (j & 1) + 1] = h1;
;                         low[j >> 1][2 * (j & 1)] = pg8::cvt_pk_bf16(h.x - bflo(h0), h.y - bfhi(h0)); low[j >> 1][2 * (j & 1) + 1] = pg8::cvt_pk_bf16(h.z - bflo(h1), h.w - bfhi(h1));
;                     }
;                     *(u32x4*)((unsigned char*)H + (size_t)row * DM + col) = h8;
; #pragma unroll
;                     for (int j = 0; j < 2; ++j) { *(LAS u32x4*)(Thi + rl * TP + col * 2 + 16 * j) = hiw[j]; *(LAS u32x4*)(Tlo + rl * TP + col * 2 + 16 * j) = low[j]; }
;                 }
	v_pk_fma_f32 v[174:175], v[162:163], v[136:137], v[114:115]
	v_mov_b32_e32 v162, v121
	v_cvt_pk_fp8_f32 v161, v172, v173 op_sel:[0,0,1]
	v_sub_f32_e32 v159, v172, v159
	v_cvt_pk_fp8_f32 v162, v174, v175
	v_pk_mul_f32 v[172:173], v[120:121], v[196:197] op_sel_hi:[0,1]
	v_cvt_pk_bf16_f32 v171, v159, v171
	v_pk_fma_f32 v[178:179], v[172:173], v[134:135], v[116:117]
	v_cvt_pk_bf16_f32 v172, v174, v175
	s_add_i32 s14, s54, s61
	v_lshlrev_b32_e32 v159, 16, v172
	v_and_b32_e32 v163, 0xffff0000, v172
	v_sub_f32_e32 v159, v174, v159
	v_sub_f32_e32 v163, v175, v163
	v_cvt_pk_bf16_f32 v173, v178, v179
	v_cvt_pk_bf16_f32 v176, v159, v163
	v_pk_mul_f32 v[174:175], v[120:121], v[182:183] op_sel_hi:[0,1]
	v_lshlrev_b32_e32 v159, 16, v173
	v_and_b32_e32 v163, 0xffff0000, v173
	v_cvt_pk_fp8_f32 v162, v178, v179 op_sel:[0,0,1]
	v_sub_f32_e32 v159, v178, v159
	v_sub_f32_e32 v177, v179, v163
	v_pk_fma_f32 v[178:179], v[174:175], v[138:139], v[106:107]
	v_mov_b32_e32 v163, v121
	v_cvt_pk_fp8_f32 v163, v178, v179
	v_pk_mul_f32 v[174:175], v[120:121], v[184:185] op_sel_hi:[0,1]
	v_cvt_pk_bf16_f32 v177, v159, v177
	v_pk_fma_f32 v[180:181], v[174:175], v[132:133], v[108:109]
	v_cvt_pk_bf16_f32 v174, v178, v179
	s_ashr_i32 s15, s14, 31
	v_and_b32_e32 v159, 0xffff0000, v174
	v_lshlrev_b32_e32 v120, 16, v174
	v_sub_f32_e32 v159, v179, v159
	v_cvt_pk_fp8_f32 v163, v180, v181 op_sel:[0,0,1]
	v_cvt_pk_bf16_f32 v175, v180, v181
	v_sub_f32_e32 v120, v178, v120
	v_cvt_pk_bf16_f32 v178, v120, v159
	v_and_b32_e32 v159, 0xffff0000, v175
	v_lshlrev_b32_e32 v120, 16, v175
	v_sub_f32_e32 v159, v181, v159
	v_sub_f32_e32 v120, v180, v120
	v_cvt_pk_bf16_f32 v179, v120, v159
	s_lshl_b64 s[34:35], s[14:15], 10
	v_add_u32_e32 v159, s57, v125
	v_lshl_add_u64 v[180:181], v[128:129], 0, s[34:35]
	ds_write_b128 v159, v[164:167]
	v_and_b32_e32 v165, 0xffff0000, v83
	global_store_dwordx4 v[180:181], v[160:163], off
	v_lshlrev_b32_e32 v164, 16, v83
	v_mul_f32_e32 v120, v165, v165
	v_and_b32_e32 v161, 0xffff0000, v82
	v_lshlrev_b32_e32 v160, 16, v82
	v_pk_fma_f32 v[166:167], v[164:165], v[164:165], v[120:121] op_sel_hi:[1,1,0]
	v_and_b32_e32 v187, 0xffff0000, v85
	v_and_b32_e32 v186, 0xffff0000, v84
	v_mul_f32_e32 v120, v161, v161
	v_lshlrev_b32_e32 v163, 16, v80
	v_lshlrev_b32_e32 v185, 16, v85
	v_lshlrev_b32_e32 v184, 16, v84
	v_pk_mul_f32 v[188:189], v[186:187], v[186:187]
	v_pk_fma_f32 v[194:195], v[160:161], v[160:161], v[120:121] op_sel_hi:[1,1,0]
	v_and_b32_e32 v181, 0xffff0000, v80
	v_pk_fma_f32 v[188:189], v[184:185], v[184:185], v[188:189]
	v_mov_b32_e32 v162, v194
	v_mov_b32_e32 v196, v166
	v_mov_b32_e32 v197, v163
	v_and_b32_e32 v191, 0xffff0000, v78
	v_mul_f32_e32 v180, v181, v181
	v_pk_add_f32 v[166:167], v[194:195], v[166:167]
	v_pk_mul_f32 v[194:195], v[162:163], v[196:197]
	v_pk_add_f32 v[188:189], v[188:189], v[188:189] op_sel:[0,1] op_sel_hi:[1,0]
	v_lshlrev_b32_e32 v190, 16, v78
	v_and_b32_e32 v193, 0xffff0000, v79
	v_mov_b32_e32 v167, v195
	v_mov_b32_e32 v189, v180
	v_mul_f32_e32 v120, v191, v191
	v_lshlrev_b32_e32 v182, 16, v81
	v_and_b32_e32 v183, 0xffff0000, v81
	v_lshlrev_b32_e32 v192, 16, v79
	v_pk_add_f32 v[166:167], v[166:167], v[188:189]
	v_pk_fma_f32 v[188:189], v[190:191], v[190:191], v[120:121] op_sel_hi:[1,1,0]
	v_mul_f32_e32 v120, v193, v193
	v_mul_f32_e32 v198, v182, v182
	v_mul_f32_e32 v199, v183, v183
	v_pk_fma_f32 v[194:195], v[192:193], v[192:193], v[120:121] op_sel_hi:[1,1,0]
	v_mov_b32_e32 v189, v198
	v_mov_b32_e32 v195, v199
	v_pk_add_f32 v[188:189], v[188:189], v[194:195]
	v_add_u32_e32 v162, s57, v148
	v_pk_add_f32 v[166:167], v[166:167], v[188:189]
	ds_write_b128 v162, v[168:171]
	ds_write_b128 v159, v[172:175] offset:16
	v_add_f32_e32 v120, v166, v167
	ds_write_b128 v162, v[176:179] offset:16
	v_mov_b32_e32 v180, v163
	v_add_f32_dpp v120, v120, v120 quad_perm:[1,0,3,2] row_mask:0xf bank_mask:0xf bound_ctrl:1
	v_mov_b32_e32 v163, v121
	s_nop 0
	v_add_f32_dpp v120, v120, v120 quad_perm:[2,3,0,1] row_mask:0xf bank_mask:0xf bound_ctrl:1
	s_nop 1
	v_add_f32_dpp v120, v120, v120 row_half_mirror row_mask:0xf bank_mask:0xf bound_ctrl:1
	s_nop 1
	v_add_f32_dpp v120, v120, v120 row_mirror row_mask:0xf bank_mask:0xf bound_ctrl:1
	s_nop 0
	v_readlane_b32 s15, v120, 16
	v_readlane_b32 s44, v120, 48
	v_readlane_b32 s34, v120, 0
	v_readlane_b32 s35, v120, 32
	v_mov_b32_e32 v166, s15
	v_mov_b32_e32 v167, s44
	v_pk_add_f32 v[166:167], s[34:35], v[166:167]
	s_add_i32 s34, s14, 1
	v_add_f32_e32 v120, v166, v167
	v_fmamk_f32 v120, v120, 0x3a800000, v154
	v_rsq_f32_e32 v120, v120
	s_ashr_i32 s35, s34, 31
	s_lshl_b64 s[34:35], s[34:35], 10
	v_pk_mul_f32 v[160:161], v[120:121], v[160:161] op_sel_hi:[0,1]
	v_pk_fma_f32 v[166:167], v[160:161], v[146:147], v[102:103]
	v_mov_b32_e32 v160, v121
	v_pk_mul_f32 v[164:165], v[120:121], v[164:165] op_sel_hi:[0,1]
	v_cvt_pk_fp8_f32 v160, v166, v167
	v_pk_fma_f32 v[170:171], v[164:165], v[144:145], v[104:105]
	v_cvt_pk_bf16_f32 v164, v166, v167
	s_nop 0
	v_and_b32_e32 v161, 0xffff0000, v164
	v_lshlrev_b32_e32 v159, 16, v164
	v_sub_f32_e32 v161, v167, v161
	v_cvt_pk_bf16_f32 v165, v170, v171
	v_sub_f32_e32 v159, v166, v159
	v_cvt_pk_bf16_f32 v168, v159, v161
	v_and_b32_e32 v161, 0xffff0000, v165
	v_mov_b32_e32 v166, v184
	v_mov_b32_e32 v167, v186
	v_lshlrev_b32_e32 v159, 16, v165
	v_sub_f32_e32 v161, v171, v161
	v_pk_mul_f32 v[166:167], v[120:121], v[166:167] op_sel_hi:[0,1]
	v_cvt_pk_fp8_f32 v160, v170, v171 op_sel:[0,0,1]
	v_sub_f32_e32 v159, v170, v159
	v_cvt_pk_bf16_f32 v169, v159, v161
	v_pk_fma_f32 v[170:171], v[166:167], v[142:143], v[110:111]
	v_mov_b32_e32 v161, v121
	v_mov_b32_e32 v186, v185
	v_cvt_pk_fp8_f32 v161, v170, v171
; __device__ __forceinline__ unsigned cvt_pk_bf16(float lo, float hi) { unsigned r; asm volatile("v_cvt_pk_bf16_f32 %0, %1, %2" : "=v"(r) : "v"(lo), "v"(hi)); return r; }
; __device__ __forceinline__ unsigned pk4_fp8(float a, float b, float c, float d) { int w = __builtin_amdgcn_cvt_pk_fp8_f32(a, b, 0, false); w = __builtin_amdgcn_cvt_pk_fp8_f32(c, d, w, true); return (unsigned)w; }
; #define LAS __attribute__((address_space(3)))
; __global__ void __launch_bounds__(NTHR, 2) mk_fwd(Args args) {
;     ...
;                 for (int rr = 0; rr < 4; ++rr) {
;                     const int rl = wave * 4 + rr, row = row0 + rl; f32x4 v[4]; float ss = 0.f;
; #pragma unroll
;                     for (int j = 0; j < 2; ++j) { const u32x4 xb = xq[rr][j]; v[2 * j] = (f32x4){bflo(xb.x), bfhi(xb.x), bflo(xb.y), bfhi(xb.y)}; v[2 * j + 1] = (f32x4){bflo(xb.z), bfhi(xb.z), bflo(xb.w), bfhi(xb.w)}; }
; #pragma unroll
;                     for (int j = 0; j < 4; ++j) ss += (v[j].x * v[j].x + v[j].y * v[j].y) + (v[j].z * v[j].z + v[j].w * v[j].w);
;                     const float rstd = __builtin_amdgcn_rsqf(wave_sum(ss) * (1.0f / DM) + EPS);
;                     u32x4 h8, hiw[2], low[2];
; #pragma unroll
;                     for (int j = 0; j < 4; ++j) {
;                         const f32x4 h = (v[j] * rstd) * gm[j] + sv[j];
;                         h8[j] = pk4_fp8(h.x, h.y, h.z, h.w);
;                         const unsigned h0 = pg8::cvt_pk_bf16(h.x, h.y), h1 = pg8::cvt_pk_bf16(h.z, h.w);
;                         hiw[j >> 1][2 * (j & 1)] = h0; hiw[j >> 1][2 * (j & 1) + 1] = h1;
;                         low[j >> 1][2 * (j & 1)] = pg8::cvt_pk_bf16(h.x - bflo(h0), h.y - bfhi(h0)); low[j >> 1][2 * (j & 1) + 1] = pg8::cvt_pk_bf16(h.z - bflo(h1), h.w - bfhi(h1));
;                     }
;                     *(u32x4*)((unsigned char*)H + (size_t)row * DM + col) = h8;
; #pragma unroll
;                     for (int j = 0; j < 2; ++j) { *(LAS u32x4*)(Thi + rl * TP + col * 2 + 16 * j) = hiw[j]; *(LAS u32x4*)(Tlo + rl * TP + col * 2 + 16 * j) = low[j]; }
;                 }
	v_pk_mul_f32 v[166:167], v[120:121], v[186:187] op_sel_hi:[0,1]
	v_pk_fma_f32 v[172:173], v[166:167], v[140:141], v[112:113]
	v_cvt_pk_bf16_f32 v166, v170, v171
	v_and_b32_e32 v187, 0xffff0000, v93
	v_lshlrev_b32_e32 v159, 16, v166
	v_and_b32_e32 v162, 0xffff0000, v166
	v_sub_f32_e32 v159, v170, v159
	v_sub_f32_e32 v162, v171, v162
	v_cvt_pk_bf16_f32 v167, v172, v173
	v_cvt_pk_bf16_f32 v170, v159, v162
	v_cvt_pk_fp8_f32 v161, v172, v173 op_sel:[0,0,1]
	v_lshlrev_b32_e32 v159, 16, v167
	v_and_b32_e32 v162, 0xffff0000, v167
	v_sub_f32_e32 v159, v172, v159
	v_sub_f32_e32 v171, v173, v162
	v_pk_mul_f32 v[172:173], v[120:121], v[190:191] op_sel_hi:[0,1]
	v_pk_fma_f32 v[174:175], v[172:173], v[136:137], v[114:115]
	v_pk_mul_f32 v[172:173], v[120:121], v[192:193] op_sel_hi:[0,1]
	v_mov_b32_e32 v162, v121
	v_cvt_pk_bf16_f32 v171, v159, v171
	v_pk_fma_f32 v[178:179], v[172:173], v[134:135], v[116:117]
	v_cvt_pk_bf16_f32 v172, v174, v175
	v_cvt_pk_fp8_f32 v162, v174, v175
	v_lshlrev_b32_e32 v159, 16, v172
	v_sub_f32_e32 v159, v174, v159
	v_and_b32_e32 v174, 0xffff0000, v172
	v_sub_f32_e32 v174, v175, v174
	v_cvt_pk_bf16_f32 v173, v178, v179
	v_cvt_pk_bf16_f32 v176, v159, v174
	v_cvt_pk_fp8_f32 v162, v178, v179 op_sel:[0,0,1]
	v_and_b32_e32 v174, 0xffff0000, v173
	v_lshlrev_b32_e32 v159, 16, v173
	v_sub_f32_e32 v177, v179, v174
	v_pk_mul_f32 v[174:175], v[120:121], v[180:181] op_sel_hi:[0,1]
	v_sub_f32_e32 v159, v178, v159
	v_pk_fma_f32 v[178:179], v[174:175], v[138:139], v[106:107]
	v_pk_mul_f32 v[174:175], v[120:121], v[182:183] op_sel_hi:[0,1]
	v_cvt_pk_fp8_f32 v163, v178, v179
	v_cvt_pk_bf16_f32 v177, v159, v177
	v_pk_fma_f32 v[180:181], v[174:175], v[132:133], v[108:109]
	v_cvt_pk_bf16_f32 v174, v178, v179
	v_and_b32_e32 v186, 0xffff0000, v92
	v_and_b32_e32 v159, 0xffff0000, v174
	v_lshlrev_b32_e32 v120, 16, v174
	v_sub_f32_e32 v159, v179, v159
	v_cvt_pk_fp8_f32 v163, v180, v181 op_sel:[0,0,1]
	v_cvt_pk_bf16_f32 v175, v180, v181
	v_sub_f32_e32 v120, v178, v120
	v_cvt_pk_bf16_f32 v178, v120, v159
	v_and_b32_e32 v159, 0xffff0000, v175
	v_lshlrev_b32_e32 v120, 16, v175
	v_sub_f32_e32 v159, v181, v159
	v_sub_f32_e32 v120, v180, v120
	v_cvt_pk_bf16_f32 v179, v120, v159
	v_add_u32_e32 v159, s58, v125
	v_lshl_add_u64 v[180:181], v[128:129], 0, s[34:35]
	ds_write_b128 v159, v[164:167]
	v_and_b32_e32 v165, 0xffff0000, v91
	global_store_dwordx4 v[180:181], v[160:163], off
	v_lshlrev_b32_e32 v164, 16, v91
	v_mul_f32_e32 v120, v165, v165
	v_and_b32_e32 v161, 0xffff0000, v90
	v_lshlrev_b32_e32 v160, 16, v90
	v_pk_fma_f32 v[166:167], v[164:165], v[164:165], v[120:121] op_sel_hi:[1,1,0]
	v_mul_f32_e32 v120, v161, v161
	v_lshlrev_b32_e32 v163, 16, v88
	v_lshlrev_b32_e32 v185, 16, v93
	v_lshlrev_b32_e32 v184, 16, v92
	v_pk_mul_f32 v[188:189], v[186:187], v[186:187]
	v_pk_fma_f32 v[194:195], v[160:161], v[160:161], v[120:121] op_sel_hi:[1,1,0]
	v_and_b32_e32 v181, 0xffff0000, v88
	v_pk_fma_f32 v[188:189], v[184:185], v[184:185], v[188:189]
	v_mov_b32_e32 v162, v194
	v_mov_b32_e32 v196, v166
	v_mov_b32_e32 v197, v163
	v_and_b32_e32 v191, 0xffff0000, v86
	v_mul_f32_e32 v180, v181, v181
	v_pk_add_f32 v[166:167], v[194:195], v[166:167]
	v_pk_mul_f32 v[194:195], v[162:163], v[196:197]
	v_pk_add_f32 v[188:189], v[188:189], v[188:189] op_sel:[0,1] op_sel_hi:[1,0]
	v_lshlrev_b32_e32 v190, 16, v86
	v_and_b32_e32 v193, 0xffff0000, v87
	v_mov_b32_e32 v167, v195
	v_mov_b32_e32 v189, v180
	v_mul_f32_e32 v120, v191, v191
	v_lshlrev_b32_e32 v182, 16, v89
	v_and_b32_e32 v183, 0xffff0000, v89
	v_lshlrev_b32_e32 v192, 16, v87
	v_pk_add_f32 v[166:167], v[166:167], v[188:189]
	v_pk_fma_f32 v[188:189], v[190:191], v[190:191], v[120:121] op_sel_hi:[1,1,0]
	v_mul_f32_e32 v120, v193, v193
	v_mul_f32_e32 v198, v182, v182
	v_mul_f32_e32 v199, v183, v183
	v_pk_fma_f32 v[194:195], v[192:193], v[192:193], v[120:121] op_sel_hi:[1,1,0]
	v_mov_b32_e32 v189, v198
	v_mov_b32_e32 v195, v199
	v_pk_add_f32 v[188:189], v[188:189], v[194:195]
	ds_write_b128 v202, v[168:171]
	ds_write_b128 v159, v[172:175] offset:16
	v_pk_add_f32 v[166:167], v[166:167], v[188:189]
	ds_write_b128 v202, v[176:179] offset:16
	v_add_f32_e32 v120, v166, v167
	v_mov_b32_e32 v180, v163
	v_mov_b32_e32 v163, v121
	v_add_f32_dpp v120, v120, v120 quad_perm:[1,0,3,2] row_mask:0xf bank_mask:0xf bound_ctrl:1
	v_lshlrev_b32_e32 v189, 16, v101
	v_lshlrev_b32_e32 v188, 16, v100
	v_add_f32_dpp v120, v120, v120 quad_perm:[2,3,0,1] row_mask:0xf bank_mask:0xf bound_ctrl:1
	v_and_b32_e32 v195, 0xffff0000, v94
	v_lshlrev_b32_e32 v194, 16, v94
	v_add_f32_dpp v120, v120, v120 row_half_mirror row_mask:0xf bank_mask:0xf bound_ctrl:1
	v_and_b32_e32 v197, 0xffff0000, v95
	v_lshlrev_b32_e32 v196, 16, v95
	v_add_f32_dpp v120, v120, v120 row_mirror row_mask:0xf bank_mask:0xf bound_ctrl:1
	s_nop 0
	v_readlane_b32 s15, v120, 16
	v_readlane_b32 s44, v120, 48
	v_readlane_b32 s34, v120, 0
	v_readlane_b32 s35, v120, 32
	v_mov_b32_e32 v166, s15
	v_mov_b32_e32 v167, s44
	v_pk_add_f32 v[166:167], s[34:35], v[166:167]
	s_add_i32 s34, s14, 2
	v_add_f32_e32 v120, v166, v167
	v_fmamk_f32 v120, v120, 0x3a800000, v154
	v_rsq_f32_e32 v120, v120
	s_ashr_i32 s35, s34, 31
	s_lshl_b64 s[34:35], s[34:35], 10
	s_add_i32 s14, s14, 3
	v_pk_mul_f32 v[160:161], v[120:121], v[160:161] op_sel_hi:[0,1]
	v_pk_fma_f32 v[166:167], v[160:161], v[146:147], v[102:103]
	v_mov_b32_e32 v160, v121
	v_cvt_pk_fp8_f32 v160, v166, v167
	v_pk_mul_f32 v[164:165], v[120:121], v[164:165] op_sel_hi:[0,1]
	v_pk_fma_f32 v[170:171], v[164:165], v[144:145], v[104:105]
	v_cvt_pk_bf16_f32 v164, v166, v167
	s_nop 0
	v_lshlrev_b32_e32 v161, 16, v164
	v_and_b32_e32 v162, 0xffff0000, v164
; __device__ __forceinline__ unsigned cvt_pk_bf16(float lo, float hi) { unsigned r; asm volatile("v_cvt_pk_bf16_f32 %0, %1, %2" : "=v"(r) : "v"(lo), "v"(hi)); return r; }
; __device__ __forceinline__ unsigned pk4_fp8(float a, float b, float c, float d) { int w = __builtin_amdgcn_cvt_pk_fp8_f32(a, b, 0, false); w = __builtin_amdgcn_cvt_pk_fp8_f32(c, d, w, true); return (unsigned)w; }
; #define LAS __attribute__((address_space(3)))
; __global__ void __launch_bounds__(NTHR, 2) mk_fwd(Args args) {
;     ...
;                 for (int rr = 0; rr < 4; ++rr) {
;                     const int rl = wave * 4 + rr, row = row0 + rl; f32x4 v[4]; float ss = 0.f;
; #pragma unroll
;                     for (int j = 0; j < 2; ++j) { const u32x4 xb = xq[rr][j]; v[2 * j] = (f32x4){bflo(xb.x), bfhi(xb.x), bflo(xb.y), bfhi(xb.y)}; v[2 * j + 1] = (f32x4){bflo(xb.z), bfhi(xb.z), bflo(xb.w), bfhi(xb.w)}; }
; #pragma unroll
;                     for (int j = 0; j < 4; ++j) ss += (v[j].x * v[j].x + v[j].y * v[j].y) + (v[j].z * v[j].z + v[j].w * v[j].w);
;                     const float rstd = __builtin_amdgcn_rsqf(wave_sum(ss) * (1.0f / DM) + EPS);
;                     u32x4 h8, hiw[2], low[2];
; #pragma unroll
;                     for (int j = 0; j < 4; ++j) {
;                         const f32x4 h = (v[j] * rstd) * gm[j] + sv[j];
;                         h8[j] = pk4_fp8(h.x, h.y, h.z, h.w);
;                         const unsigned h0 = pg8::cvt_pk_bf16(h.x, h.y), h1 = pg8::cvt_pk_bf16(h.z, h.w);
;                         hiw[j >> 1][2 * (j & 1)] = h0; hiw[j >> 1][2 * (j & 1) + 1] = h1;
;                         low[j >> 1][2 * (j & 1)] = pg8::cvt_pk_bf16(h.x - bflo(h0), h.y - bfhi(h0)); low[j >> 1][2 * (j & 1) + 1] = pg8::cvt_pk_bf16(h.z - bflo(h1), h.w - bfhi(h1));
;                     }
;                     *(u32x4*)((unsigned char*)H + (size_t)row * DM + col) = h8;
; #pragma unroll
;                     for (int j = 0; j < 2; ++j) { *(LAS u32x4*)(Thi + rl * TP + col * 2 + 16 * j) = hiw[j]; *(LAS u32x4*)(Tlo + rl * TP + col * 2 + 16 * j) = low[j]; }
;                 }
	v_sub_f32_e32 v161, v166, v161
	v_sub_f32_e32 v162, v167, v162
	v_mov_b32_e32 v166, v184
	v_mov_b32_e32 v167, v186
	v_cvt_pk_bf16_f32 v165, v170, v171
	v_cvt_pk_bf16_f32 v168, v161, v162
	v_pk_mul_f32 v[166:167], v[120:121], v[166:167] op_sel_hi:[0,1]
	v_lshlrev_b32_e32 v161, 16, v165
	v_and_b32_e32 v162, 0xffff0000, v165
	v_mov_b32_e32 v186, v185
	v_cvt_pk_fp8_f32 v160, v170, v171 op_sel:[0,0,1]
	v_sub_f32_e32 v161, v170, v161
	v_sub_f32_e32 v162, v171, v162
	v_pk_fma_f32 v[170:171], v[166:167], v[142:143], v[110:111]
	v_pk_mul_f32 v[166:167], v[120:121], v[186:187] op_sel_hi:[0,1]
	v_cvt_pk_bf16_f32 v169, v161, v162
	v_mov_b32_e32 v161, v121
	v_pk_fma_f32 v[172:173], v[166:167], v[140:141], v[112:113]
	v_cvt_pk_bf16_f32 v166, v170, v171
	v_cvt_pk_fp8_f32 v161, v170, v171
	v_lshlrev_b32_e32 v162, 16, v166
	v_sub_f32_e32 v162, v170, v162
	v_and_b32_e32 v170, 0xffff0000, v166
	v_sub_f32_e32 v170, v171, v170
	v_cvt_pk_bf16_f32 v167, v172, v173
	v_cvt_pk_bf16_f32 v170, v162, v170
	v_cvt_pk_fp8_f32 v161, v172, v173 op_sel:[0,0,1]
	v_lshlrev_b32_e32 v162, 16, v167
	v_sub_f32_e32 v171, v172, v162
	v_and_b32_e32 v162, 0xffff0000, v167
	v_sub_f32_e32 v176, v173, v162
	v_pk_mul_f32 v[172:173], v[120:121], v[190:191] op_sel_hi:[0,1]
	v_pk_fma_f32 v[174:175], v[172:173], v[136:137], v[114:115]
	v_pk_mul_f32 v[172:173], v[120:121], v[192:193] op_sel_hi:[0,1]
	v_mov_b32_e32 v162, v121
	v_cvt_pk_bf16_f32 v171, v171, v176
	v_pk_fma_f32 v[178:179], v[172:173], v[134:135], v[116:117]
	v_cvt_pk_bf16_f32 v172, v174, v175
	v_cvt_pk_fp8_f32 v162, v174, v175
	v_lshlrev_b32_e32 v176, 16, v172
	v_sub_f32_e32 v174, v174, v176
	v_and_b32_e32 v176, 0xffff0000, v172
	v_cvt_pk_bf16_f32 v173, v178, v179
	v_sub_f32_e32 v175, v175, v176
	v_cvt_pk_bf16_f32 v176, v174, v175
	v_lshlrev_b32_e32 v174, 16, v173
	v_sub_f32_e32 v177, v178, v174
	v_and_b32_e32 v174, 0xffff0000, v173
	v_sub_f32_e32 v184, v179, v174
	v_pk_mul_f32 v[174:175], v[120:121], v[180:181] op_sel_hi:[0,1]
	v_cvt_pk_fp8_f32 v162, v178, v179 op_sel:[0,0,1]
	v_pk_fma_f32 v[178:179], v[174:175], v[138:139], v[106:107]
	v_pk_mul_f32 v[174:175], v[120:121], v[182:183] op_sel_hi:[0,1]
	v_cvt_pk_fp8_f32 v163, v178, v179
	v_cvt_pk_bf16_f32 v177, v177, v184
	v_pk_fma_f32 v[180:181], v[174:175], v[132:133], v[108:109]
	v_cvt_pk_bf16_f32 v174, v178, v179
	v_and_b32_e32 v191, 0xffff0000, v101
	v_lshlrev_b32_e32 v120, 16, v174
	v_cvt_pk_fp8_f32 v163, v180, v181 op_sel:[0,0,1]
	v_sub_f32_e32 v120, v178, v120
	v_and_b32_e32 v178, 0xffff0000, v174
	v_sub_f32_e32 v178, v179, v178
	v_cvt_pk_bf16_f32 v175, v180, v181
	v_cvt_pk_bf16_f32 v178, v120, v178
	v_and_b32_e32 v190, 0xffff0000, v100
	v_lshlrev_b32_e32 v120, 16, v175
	v_and_b32_e32 v179, 0xffff0000, v175
	v_sub_f32_e32 v120, v180, v120
	v_sub_f32_e32 v179, v181, v179
	v_lshl_add_u64 v[180:181], v[128:129], 0, s[34:35]
	v_cvt_pk_bf16_f32 v179, v120, v179
	global_store_dwordx4 v[180:181], v[160:163], off
	v_lshlrev_b32_e32 v181, 16, v96
	v_pk_mul_f32 v[192:193], v[190:191], v[190:191]
	v_and_b32_e32 v163, 0xffff0000, v99
	v_and_b32_e32 v161, 0xffff0000, v98
	v_lshlrev_b32_e32 v162, 16, v99
	v_mul_f32_e32 v120, v163, v163
	v_lshlrev_b32_e32 v160, 16, v98
	v_pk_fma_f32 v[186:187], v[162:163], v[162:163], v[120:121] op_sel_hi:[1,1,0]
	v_mul_f32_e32 v120, v161, v161
	v_pk_fma_f32 v[198:199], v[160:161], v[160:161], v[120:121] op_sel_hi:[1,1,0]
	v_and_b32_e32 v183, 0xffff0000, v96
	v_pk_fma_f32 v[192:193], v[188:189], v[188:189], v[192:193]
	v_mov_b32_e32 v180, v198
	v_mov_b32_e32 v200, v186
	v_mov_b32_e32 v201, v181
	v_mul_f32_e32 v182, v183, v183
	v_pk_add_f32 v[186:187], v[198:199], v[186:187]
	v_pk_mul_f32 v[198:199], v[180:181], v[200:201]
	v_pk_add_f32 v[192:193], v[192:193], v[192:193] op_sel:[0,1] op_sel_hi:[1,0]
	v_mov_b32_e32 v187, v199
	v_mov_b32_e32 v193, v182
	v_mul_f32_e32 v120, v195, v195
	v_lshlrev_b32_e32 v184, 16, v97
	v_and_b32_e32 v185, 0xffff0000, v97
	v_pk_add_f32 v[186:187], v[186:187], v[192:193]
	v_pk_fma_f32 v[192:193], v[194:195], v[194:195], v[120:121] op_sel_hi:[1,1,0]
	v_mul_f32_e32 v120, v197, v197
	v_mul_f32_e32 v203, v184, v184
	v_mul_f32_e32 v204, v185, v185
	v_pk_fma_f32 v[198:199], v[196:197], v[196:197], v[120:121] op_sel_hi:[1,1,0]
	v_mov_b32_e32 v193, v203
	v_mov_b32_e32 v199, v204
	v_pk_add_f32 v[192:193], v[192:193], v[198:199]
	ds_write_b128 v159, v[164:167] offset:2064
	ds_write_b128 v202, v[168:171] offset:2064
	ds_write_b128 v159, v[172:175] offset:2080
	v_pk_add_f32 v[186:187], v[186:187], v[192:193]
	ds_write_b128 v202, v[176:179] offset:2080
	v_add_f32_e32 v120, v186, v187
	v_mov_b32_e32 v182, v181
	s_nop 0
	v_add_f32_dpp v120, v120, v120 quad_perm:[1,0,3,2] row_mask:0xf bank_mask:0xf bound_ctrl:1
	s_nop 1
	v_add_f32_dpp v120, v120, v120 quad_perm:[2,3,0,1] row_mask:0xf bank_mask:0xf bound_ctrl:1
	s_nop 1
	v_add_f32_dpp v120, v120, v120 row_half_mirror row_mask:0xf bank_mask:0xf bound_ctrl:1
	s_nop 1
	v_add_f32_dpp v120, v120, v120 row_mirror row_mask:0xf bank_mask:0xf bound_ctrl:1
	s_nop 0
	v_readlane_b32 s15, v120, 16
	v_readlane_b32 s44, v120, 48
	v_readlane_b32 s34, v120, 0
	v_readlane_b32 s35, v120, 32
	v_mov_b32_e32 v186, s15
	v_mov_b32_e32 v187, s44
	v_pk_add_f32 v[186:187], s[34:35], v[186:187]
	s_ashr_i32 s15, s14, 31
	v_add_f32_e32 v120, v186, v187
	v_fmamk_f32 v120, v120, 0x3a800000, v154
	v_rsq_f32_e32 v120, v120
	s_lshl_b64 s[14:15], s[14:15], 10
	s_cmpk_gt_i32 s65, 0x7ff
	s_cselect_b64 s[34:35], -1, 0
	v_pk_mul_f32 v[160:161], v[120:121], v[160:161] op_sel_hi:[0,1]
	v_pk_fma_f32 v[146:147], v[160:161], v[146:147], v[102:103]
	v_mov_b32_e32 v102, v121
	v_cvt_pk_fp8_f32 v102, v146, v147
; __device__ __forceinline__ unsigned cvt_pk_bf16(float lo, float hi) { unsigned r; asm volatile("v_cvt_pk_bf16_f32 %0, %1, %2" : "=v"(r) : "v"(lo), "v"(hi)); return r; }
; __device__ __forceinline__ unsigned pk4_fp8(float a, float b, float c, float d) { int w = __builtin_amdgcn_cvt_pk_fp8_f32(a, b, 0, false); w = __builtin_amdgcn_cvt_pk_fp8_f32(c, d, w, true); return (unsigned)w; }
; #define LAS __attribute__((address_space(3)))
; __global__ void __launch_bounds__(NTHR, 2) mk_fwd(Args args) {
;     ...
;                     for (int j = 0; j < 4; ++j) {
;                         const f32x4 h = (v[j] * rstd) * gm[j] + sv[j];
;                         h8[j] = pk4_fp8(h.x, h.y, h.z, h.w);
;                         const unsigned h0 = pg8::cvt_pk_bf16(h.x, h.y), h1 = pg8::cvt_pk_bf16(h.z, h.w);
;                         hiw[j >> 1][2 * (j & 1)] = h0; hiw[j >> 1][2 * (j & 1) + 1] = h1;
;                         low[j >> 1][2 * (j & 1)] = pg8::cvt_pk_bf16(h.x - bflo(h0), h.y - bfhi(h0)); low[j >> 1][2 * (j & 1) + 1] = pg8::cvt_pk_bf16(h.z - bflo(h1), h.w - bfhi(h1));
;                     }
;                     *(u32x4*)((unsigned char*)H + (size_t)row * DM + col) = h8;
; #pragma unroll
;                     for (int j = 0; j < 2; ++j) { *(LAS u32x4*)(Thi + rl * TP + col * 2 + 16 * j) = hiw[j]; *(LAS u32x4*)(Tlo + rl * TP + col * 2 + 16 * j) = low[j]; }
;                 }
;                 __syncthreads();
;                 if (grp + G < nmoe / 32) {
; #pragma unroll
;                     for (int rr = 0; rr < 4; ++rr)
; #pragma unroll
;                         for (int j = 0; j < 2; ++j) xq[rr][j] = *(const u32x4*)(X1 + (size_t)((grp + G) * 32 + wave * 4 + rr) * DM + lane * 16 + 8 * j);
;                 }
	v_pk_mul_f32 v[160:161], v[120:121], v[162:163] op_sel_hi:[0,1]
	v_pk_fma_f32 v[104:105], v[160:161], v[144:145], v[104:105]
	v_cvt_pk_bf16_f32 v144, v146, v147
	s_and_b64 vcc, exec, s[34:35]
	v_lshlrev_b32_e32 v103, 16, v144
	v_sub_f32_e32 v103, v146, v103
	v_and_b32_e32 v146, 0xffff0000, v144
	v_cvt_pk_bf16_f32 v145, v104, v105
	v_sub_f32_e32 v146, v147, v146
	v_cvt_pk_bf16_f32 v160, v103, v146
	v_lshlrev_b32_e32 v103, 16, v145
	v_cvt_pk_fp8_f32 v102, v104, v105 op_sel:[0,0,1]
	v_sub_f32_e32 v103, v104, v103
	v_and_b32_e32 v104, 0xffff0000, v145
	v_sub_f32_e32 v104, v105, v104
	v_cvt_pk_bf16_f32 v161, v103, v104
	v_mov_b32_e32 v104, v188
	v_mov_b32_e32 v105, v190
	v_pk_mul_f32 v[104:105], v[120:121], v[104:105] op_sel_hi:[0,1]
	v_pk_fma_f32 v[104:105], v[104:105], v[142:143], v[110:111]
	v_mov_b32_e32 v103, v121
	v_mov_b32_e32 v190, v189
	v_cvt_pk_fp8_f32 v103, v104, v105
	v_pk_mul_f32 v[110:111], v[120:121], v[190:191] op_sel_hi:[0,1]
	v_pk_fma_f32 v[110:111], v[110:111], v[140:141], v[112:113]
	v_cvt_pk_bf16_f32 v146, v104, v105
	s_nop 0
	v_lshlrev_b32_e32 v112, 16, v146
	v_sub_f32_e32 v104, v104, v112
	v_and_b32_e32 v112, 0xffff0000, v146
	v_cvt_pk_bf16_f32 v147, v110, v111
	v_sub_f32_e32 v105, v105, v112
	v_cvt_pk_bf16_f32 v162, v104, v105
	v_lshlrev_b32_e32 v104, 16, v147
	v_cvt_pk_fp8_f32 v103, v110, v111 op_sel:[0,0,1]
	v_sub_f32_e32 v110, v110, v104
	v_and_b32_e32 v104, 0xffff0000, v147
	v_sub_f32_e32 v111, v111, v104
	v_pk_mul_f32 v[104:105], v[120:121], v[194:195] op_sel_hi:[0,1]
	v_pk_fma_f32 v[112:113], v[104:105], v[136:137], v[114:115]
	v_mov_b32_e32 v104, v121
	v_cvt_pk_bf16_f32 v163, v110, v111
	v_pk_mul_f32 v[110:111], v[120:121], v[196:197] op_sel_hi:[0,1]
	v_cvt_pk_fp8_f32 v104, v112, v113
	v_pk_fma_f32 v[116:117], v[110:111], v[134:135], v[116:117]
	v_cvt_pk_bf16_f32 v110, v112, v113
	s_nop 0
	v_lshlrev_b32_e32 v105, 16, v110
	v_sub_f32_e32 v105, v112, v105
	v_and_b32_e32 v112, 0xffff0000, v110
	v_cvt_pk_bf16_f32 v111, v116, v117
	v_sub_f32_e32 v112, v113, v112
	v_cvt_pk_bf16_f32 v114, v105, v112
	v_lshlrev_b32_e32 v105, 16, v111
	v_sub_f32_e32 v115, v116, v105
	v_and_b32_e32 v105, 0xffff0000, v111
	v_pk_mul_f32 v[112:113], v[120:121], v[182:183] op_sel_hi:[0,1]
	v_cvt_pk_fp8_f32 v104, v116, v117 op_sel:[0,0,1]
	v_sub_f32_e32 v116, v117, v105
	v_pk_fma_f32 v[106:107], v[112:113], v[138:139], v[106:107]
	v_mov_b32_e32 v105, v121
	v_cvt_pk_fp8_f32 v105, v106, v107
	v_pk_mul_f32 v[112:113], v[120:121], v[184:185] op_sel_hi:[0,1]
	v_cvt_pk_bf16_f32 v115, v115, v116
	v_pk_fma_f32 v[108:109], v[112:113], v[132:133], v[108:109]
	v_cvt_pk_bf16_f32 v112, v106, v107
	s_nop 0
	v_lshlrev_b32_e32 v116, 16, v112
	v_sub_f32_e32 v106, v106, v116
	v_and_b32_e32 v116, 0xffff0000, v112
	v_cvt_pk_fp8_f32 v105, v108, v109 op_sel:[0,0,1]
	v_sub_f32_e32 v107, v107, v116
	v_cvt_pk_bf16_f32 v113, v108, v109
	v_cvt_pk_bf16_f32 v116, v106, v107
	s_nop 0
	v_lshlrev_b32_e32 v106, 16, v113
	v_and_b32_e32 v107, 0xffff0000, v113
	v_sub_f32_e32 v106, v108, v106
	v_sub_f32_e32 v107, v109, v107
	v_cvt_pk_bf16_f32 v117, v106, v107
	v_lshl_add_u64 v[106:107], v[128:129], 0, s[14:15]
	global_store_dwordx4 v[106:107], v[102:105], off
	ds_write_b128 v159, v[144:147] offset:4128
	ds_write_b128 v202, v[160:163] offset:4128
	ds_write_b128 v159, v[110:113] offset:4144
	ds_write_b128 v202, v[114:117] offset:4144
	s_waitcnt lgkmcnt(0)
	s_barrier
	global_load_dwordx4 v[176:179], v[122:123], off offset:768
	global_load_dwordx4 v[180:183], v[122:123], off offset:832
	global_load_dwordx4 v[184:187], v[122:123], off offset:896
	global_load_dwordx4 v[188:191], v[122:123], off offset:960
	s_add_i32 s14, s54, s59
	s_ashr_i32 s15, s14, 31
	s_lshl_b64 s[44:45], s[14:15], 11
	v_lshl_add_u64 v[74:75], v[130:131], 0, s[44:45]
	s_add_i32 s44, s14, 1
	s_ashr_i32 s45, s44, 31
	s_lshl_b64 s[44:45], s[44:45], 11
	v_lshl_add_u64 v[82:83], v[130:131], 0, s[44:45]
	s_add_i32 s44, s14, 2
	s_add_i32 s14, s14, 3
	s_ashr_i32 s45, s44, 31
	s_ashr_i32 s15, s14, 31
	s_lshl_b64 s[44:45], s[44:45], 11
	s_lshl_b64 s[14:15], s[14:15], 11
	v_lshl_add_u64 v[90:91], v[130:131], 0, s[44:45]
	v_lshl_add_u64 v[98:99], v[130:131], 0, s[14:15]
	global_load_dwordx4 v[70:73], v[74:75], off offset:16
	s_nop 0
	global_load_dwordx4 v[74:77], v[74:75], off
	s_nop 0
	global_load_dwordx4 v[78:81], v[82:83], off offset:16
	s_nop 0
	global_load_dwordx4 v[82:85], v[82:83], off
	s_nop 0
	global_load_dwordx4 v[86:89], v[90:91], off offset:16
	s_nop 0
	global_load_dwordx4 v[90:93], v[90:91], off
	s_nop 0
	global_load_dwordx4 v[94:97], v[98:99], off offset:16
	s_nop 0
	global_load_dwordx4 v[98:101], v[98:99], off
; #define LAS __attribute__((address_space(3)))
; __global__ void __launch_bounds__(NTHR, 2) mk_fwd(Args args) {
;     ...
;                 f32x4 acc = (f32x4){0.f, 0.f, 0.f, 0.f};
; #pragma unroll
;                 for (int st = 0; st < 16; ++st) {
;                     const int kb = (kh * 512 + 32 * st + 8 * q4) * 2;
;                     const fa::bf16x8 bh = *(const LAS fa::bf16x8*)(Thi + (rh * 16 + n16) * TP + kb), bl = *(const LAS fa::bf16x8*)(Tlo + (rh * 16 + n16) * TP + kb);
;                     acc = __builtin_amdgcn_mfma_f32_16x16x32_bf16(ah[st], bh, acc, 0, 0, 0);
;                     acc = __builtin_amdgcn_mfma_f32_16x16x32_bf16(ah[st], bl, acc, 0, 0, 0);
;                     acc = __builtin_amdgcn_mfma_f32_16x16x32_bf16(*(const fa::bf16x8*)(alp + 32 * st), bh, acc, 0, 0, 0);
;                 }
;                 if (kh == 1) *(LAS f32x4*)(PART + (wave & 3) * 1024 + lane * 16) = acc;
.LBB0_1570:
	s_nop 0
	s_andn2_b64 vcc, exec, s[24:25]
	ds_read_b128 v[106:109], v155
	ds_read_b128 v[132:135], v156
	ds_read_b128 v[110:113], v155 offset:64
	ds_read_b128 v[136:139], v156 offset:64
	ds_read_b128 v[114:117], v155 offset:128
	ds_read_b128 v[140:143], v156 offset:128
	s_waitcnt lgkmcnt(5)
	v_mfma_f32_16x16x32_bf16 v[102:105], v[58:61], v[106:109], 0
	s_waitcnt lgkmcnt(4)
	v_mfma_f32_16x16x32_bf16 v[102:105], v[58:61], v[132:135], v[102:105]
	v_mfma_f32_16x16x32_bf16 v[102:105], v[206:209], v[106:109], v[102:105]
	ds_read_b128 v[106:109], v155 offset:192
	ds_read_b128 v[132:135], v156 offset:192
	s_waitcnt lgkmcnt(5)
	v_mfma_f32_16x16x32_bf16 v[102:105], v[2:5], v[110:113], v[102:105]
	s_waitcnt lgkmcnt(4)
	v_mfma_f32_16x16x32_bf16 v[102:105], v[2:5], v[136:139], v[102:105]
	v_mfma_f32_16x16x32_bf16 v[102:105], v[210:213], v[110:113], v[102:105]
	ds_read_b128 v[110:113], v155 offset:256
	ds_read_b128 v[136:139], v156 offset:256
	s_waitcnt lgkmcnt(5)
	v_mfma_f32_16x16x32_bf16 v[102:105], v[6:9], v[114:117], v[102:105]
	s_waitcnt lgkmcnt(4)
	v_mfma_f32_16x16x32_bf16 v[102:105], v[6:9], v[140:143], v[102:105]
	v_mfma_f32_16x16x32_bf16 v[102:105], v[214:217], v[114:117], v[102:105]
	ds_read_b128 v[114:117], v155 offset:320
	ds_read_b128 v[140:143], v156 offset:320
	s_waitcnt lgkmcnt(5)
	v_mfma_f32_16x16x32_bf16 v[102:105], v[10:13], v[106:109], v[102:105]
	s_waitcnt lgkmcnt(4)
	v_mfma_f32_16x16x32_bf16 v[102:105], v[10:13], v[132:135], v[102:105]
	v_mfma_f32_16x16x32_bf16 v[102:105], v[218:221], v[106:109], v[102:105]
	ds_read_b128 v[106:109], v155 offset:384
	ds_read_b128 v[132:135], v156 offset:384
	s_waitcnt lgkmcnt(5)
	v_mfma_f32_16x16x32_bf16 v[102:105], v[14:17], v[110:113], v[102:105]
	s_waitcnt lgkmcnt(4)
	v_mfma_f32_16x16x32_bf16 v[102:105], v[14:17], v[136:139], v[102:105]
	v_mfma_f32_16x16x32_bf16 v[102:105], v[222:225], v[110:113], v[102:105]
	ds_read_b128 v[110:113], v155 offset:448
	ds_read_b128 v[136:139], v156 offset:448
	s_waitcnt lgkmcnt(5)
	v_mfma_f32_16x16x32_bf16 v[102:105], v[18:21], v[114:117], v[102:105]
	s_waitcnt lgkmcnt(4)
	v_mfma_f32_16x16x32_bf16 v[102:105], v[18:21], v[140:143], v[102:105]
	v_mfma_f32_16x16x32_bf16 v[102:105], v[226:229], v[114:117], v[102:105]
	ds_read_b128 v[114:117], v155 offset:512
	ds_read_b128 v[140:143], v156 offset:512
	s_waitcnt lgkmcnt(5)
	v_mfma_f32_16x16x32_bf16 v[102:105], v[22:25], v[106:109], v[102:105]
	s_waitcnt lgkmcnt(4)
	v_mfma_f32_16x16x32_bf16 v[102:105], v[22:25], v[132:135], v[102:105]
	v_mfma_f32_16x16x32_bf16 v[102:105], v[230:233], v[106:109], v[102:105]
	ds_read_b128 v[106:109], v155 offset:576
	ds_read_b128 v[132:135], v156 offset:576
	s_waitcnt lgkmcnt(5)
	v_mfma_f32_16x16x32_bf16 v[102:105], v[26:29], v[110:113], v[102:105]
	s_waitcnt lgkmcnt(4)
	v_mfma_f32_16x16x32_bf16 v[102:105], v[26:29], v[136:139], v[102:105]
	v_mfma_f32_16x16x32_bf16 v[102:105], v[234:237], v[110:113], v[102:105]
	ds_read_b128 v[110:113], v155 offset:640
	ds_read_b128 v[136:139], v156 offset:640
	s_waitcnt lgkmcnt(5)
	v_mfma_f32_16x16x32_bf16 v[102:105], v[30:33], v[114:117], v[102:105]
	s_waitcnt lgkmcnt(4)
	v_mfma_f32_16x16x32_bf16 v[102:105], v[30:33], v[140:143], v[102:105]
	v_mfma_f32_16x16x32_bf16 v[102:105], v[238:241], v[114:117], v[102:105]
	ds_read_b128 v[114:117], v155 offset:704
	ds_read_b128 v[140:143], v156 offset:704
	s_waitcnt lgkmcnt(5)
	v_mfma_f32_16x16x32_bf16 v[102:105], v[34:37], v[106:109], v[102:105]
	s_waitcnt lgkmcnt(4)
	v_mfma_f32_16x16x32_bf16 v[102:105], v[34:37], v[132:135], v[102:105]
	v_mfma_f32_16x16x32_bf16 v[102:105], v[242:245], v[106:109], v[102:105]
	ds_read_b128 v[106:109], v155 offset:768
	ds_read_b128 v[132:135], v156 offset:768
	s_waitcnt lgkmcnt(5)
	v_mfma_f32_16x16x32_bf16 v[102:105], v[38:41], v[110:113], v[102:105]
	s_waitcnt lgkmcnt(4)
	v_mfma_f32_16x16x32_bf16 v[102:105], v[38:41], v[136:139], v[102:105]
	v_mfma_f32_16x16x32_bf16 v[102:105], v[246:249], v[110:113], v[102:105]
	ds_read_b128 v[110:113], v155 offset:832
	ds_read_b128 v[136:139], v156 offset:832
	s_waitcnt lgkmcnt(5)
	v_mfma_f32_16x16x32_bf16 v[102:105], v[42:45], v[114:117], v[102:105]
	s_waitcnt lgkmcnt(4)
	v_mfma_f32_16x16x32_bf16 v[102:105], v[42:45], v[140:143], v[102:105]
	v_mfma_f32_16x16x32_bf16 v[102:105], v[250:253], v[114:117], v[102:105]
	ds_read_b128 v[114:117], v155 offset:896
	ds_read_b128 v[140:143], v156 offset:896
	s_waitcnt lgkmcnt(5)
	v_mfma_f32_16x16x32_bf16 v[102:105], v[46:49], v[106:109], v[102:105]
	s_waitcnt lgkmcnt(4)
	v_mfma_f32_16x16x32_bf16 v[102:105], v[46:49], v[132:135], v[102:105]
	s_waitcnt vmcnt(11)
	v_mfma_f32_16x16x32_bf16 v[102:105], v[176:179], v[106:109], v[102:105]
	ds_read_b128 v[106:109], v155 offset:960
	ds_read_b128 v[132:135], v156 offset:960
	s_waitcnt lgkmcnt(5)
	v_mfma_f32_16x16x32_bf16 v[102:105], v[50:53], v[110:113], v[102:105]
	s_waitcnt lgkmcnt(4)
	v_mfma_f32_16x16x32_bf16 v[102:105], v[50:53], v[136:139], v[102:105]
	s_waitcnt vmcnt(10)
	v_mfma_f32_16x16x32_bf16 v[102:105], v[180:183], v[110:113], v[102:105]
	s_waitcnt lgkmcnt(3)
	v_mfma_f32_16x16x32_bf16 v[102:105], v[54:57], v[114:117], v[102:105]
	s_waitcnt lgkmcnt(2)
	v_mfma_f32_16x16x32_bf16 v[102:105], v[54:57], v[140:143], v[102:105]
	s_waitcnt vmcnt(9)
	v_mfma_f32_16x16x32_bf16 v[102:105], v[184:187], v[114:117], v[102:105]
	s_waitcnt lgkmcnt(1)
	v_mfma_f32_16x16x32_bf16 v[102:105], v[62:65], v[106:109], v[102:105]
	s_waitcnt lgkmcnt(0)
	v_mfma_f32_16x16x32_bf16 v[102:105], v[62:65], v[132:135], v[102:105]
	s_waitcnt vmcnt(8)
	v_mfma_f32_16x16x32_bf16 v[102:105], v[188:191], v[106:109], v[102:105]
	s_cbranch_vccnz .LBB0_1572
	v_add_u32_e32 v106, s55, v124
	s_nop 5
	ds_write_b128 v106, v[102:105]
